# prologue phase: the 8-byte-per-lane converted-weight stores (partial lines) lose their nt hint so they merge in L2 before write-back
# speedup vs baseline: 1.0152x; 1.0152x over previous
.LBB0_254:
	s_andn2_b64 vcc, exec, s[2:3]
	s_cbranch_vccnz .LBB0_256
	s_and_b32 s2, s80, 0x3fc0
	s_add_i32 s34, s2, 0xffffc800
	s_lshl_b64 s[2:3], s[34:35], 13
	s_add_u32 s2, s46, s2
	s_addc_u32 s3, s47, s3
	s_and_b32 s4, s95, 0x7c0
	s_lshl_b32 s5, s4, 2
	s_add_u32 s2, s2, s5
	s_addc_u32 s3, s3, 0
	v_lshl_add_u64 v[132:133], s[2:3], 0, v[10:11]
	v_add_co_u32_e32 v76, vcc, s88, v132
	s_mov_b32 s2, 0x28000
	s_nop 0
	v_addc_co_u32_e32 v77, vcc, 0, v133, vcc
	v_add_co_u32_e32 v80, vcc, s89, v132
	global_load_dwordx4 v[40:43], v[132:133], off nt
	s_nop 0
	global_load_dwordx4 v[76:79], v[76:77], off nt
	v_addc_co_u32_e32 v81, vcc, 0, v133, vcc
	v_add_co_u32_e32 v84, vcc, s90, v132
	v_add_u32_e32 v1, 0x410, v48
	s_nop 0
	v_addc_co_u32_e32 v85, vcc, 0, v133, vcc
	global_load_dwordx4 v[80:83], v[80:81], off nt
	s_nop 0
	global_load_dwordx4 v[84:87], v[84:85], off nt
	v_add_co_u32_e32 v88, vcc, s91, v132
	v_readlane_b32 s3, v255, 21
	s_nop 0
	v_addc_co_u32_e32 v89, vcc, 0, v133, vcc
	v_add_co_u32_e32 v92, vcc, s2, v132
	s_mov_b32 s2, 0x30000
	s_nop 0
	v_addc_co_u32_e32 v93, vcc, 0, v133, vcc
	global_load_dwordx4 v[88:91], v[88:89], off nt
	s_nop 0
	global_load_dwordx4 v[92:95], v[92:93], off nt
	v_add_co_u32_e32 v96, vcc, s2, v132
	s_lshl_b32 s2, s4, 9
	s_nop 0
	v_addc_co_u32_e32 v97, vcc, 0, v133, vcc
	v_add_co_u32_e32 v100, vcc, s94, v132
	s_add_u32 s2, s3, s2
	s_nop 0
	v_addc_co_u32_e32 v101, vcc, 0, v133, vcc
	global_load_dwordx4 v[96:99], v[96:97], off nt
	s_nop 0
	global_load_dwordx4 v[100:103], v[100:101], off nt
	v_add_co_u32_e32 v104, vcc, s1, v132
	v_readlane_b32 s3, v255, 22
	s_nop 0
	v_addc_co_u32_e32 v105, vcc, 0, v133, vcc
	v_add_co_u32_e32 v108, vcc, s0, v132
	s_addc_u32 s3, s3, 0
	s_nop 0
	v_addc_co_u32_e32 v109, vcc, 0, v133, vcc
	global_load_dwordx4 v[104:107], v[104:105], off nt
	s_nop 0
	global_load_dwordx4 v[108:111], v[108:109], off nt
	v_add_co_u32_e32 v112, vcc, s78, v132
	s_add_u32 s2, s2, s34
	s_nop 0
	v_addc_co_u32_e32 v113, vcc, 0, v133, vcc
	v_add_co_u32_e32 v116, vcc, s79, v132
	s_addc_u32 s3, s3, 0
	s_nop 0
	v_addc_co_u32_e32 v117, vcc, 0, v133, vcc
	global_load_dwordx4 v[112:115], v[112:113], off nt
	s_nop 0
	global_load_dwordx4 v[116:119], v[116:117], off nt
	v_add_co_u32_e32 v120, vcc, s30, v132
	s_nop 1
	v_addc_co_u32_e32 v121, vcc, 0, v133, vcc
	v_add_co_u32_e32 v124, vcc, s31, v132
	s_nop 1
	v_addc_co_u32_e32 v125, vcc, 0, v133, vcc
	global_load_dwordx4 v[120:123], v[120:121], off nt
	s_nop 0
	global_load_dwordx4 v[124:127], v[124:125], off nt
	v_add_co_u32_e32 v128, vcc, s73, v132
	s_nop 1
	v_addc_co_u32_e32 v129, vcc, 0, v133, vcc
	global_load_dwordx4 v[128:131], v[128:129], off nt
	v_add_co_u32_e32 v132, vcc, s77, v132
	s_nop 1
	v_addc_co_u32_e32 v133, vcc, 0, v133, vcc
	global_load_dwordx4 v[132:135], v[132:133], off nt
	s_waitcnt vmcnt(15)
	ds_write2_b32 v48, v40, v41 offset1:1
	ds_write2_b32 v48, v42, v43 offset0:2 offset1:3
	s_waitcnt vmcnt(14)
	ds_write2_b32 v1, v76, v77 offset1:1
	v_add_u32_e32 v1, 0x418, v48
	ds_write2_b32 v1, v78, v79 offset1:1
	v_add_u32_e32 v1, 0x820, v48
	s_waitcnt vmcnt(13)
	ds_write2_b32 v1, v80, v81 offset1:1
	v_add_u32_e32 v1, 0x828, v48
	ds_write2_b32 v1, v82, v83 offset1:1
	v_add_u32_e32 v1, 0xc30, v48
	s_waitcnt vmcnt(12)
	ds_write2_b32 v1, v84, v85 offset1:1
	v_add_u32_e32 v1, 0xc38, v48
	ds_write2_b32 v1, v86, v87 offset1:1
	v_add_u32_e32 v1, 0x1040, v48
	s_waitcnt vmcnt(11)
	ds_write2_b32 v1, v88, v89 offset1:1
	v_add_u32_e32 v1, 0x1048, v48
	ds_write2_b32 v1, v90, v91 offset1:1
	v_add_u32_e32 v1, 0x1450, v48
	s_waitcnt vmcnt(10)
	ds_write2_b32 v1, v92, v93 offset1:1
	v_add_u32_e32 v1, 0x1458, v48
	ds_write2_b32 v1, v94, v95 offset1:1
	v_add_u32_e32 v1, 0x1860, v48
	v_mov_b32_e32 v90, v3
	v_mov_b32_e32 v91, v3
	v_mov_b32_e32 v92, v3
	s_waitcnt vmcnt(9)
	ds_write2_b32 v1, v96, v97 offset1:1
	v_add_u32_e32 v1, 0x1868, v48
	ds_write2_b32 v1, v98, v99 offset1:1
	v_add_u32_e32 v1, 0x1c70, v48
	s_waitcnt vmcnt(8)
	ds_write2_b32 v1, v100, v101 offset1:1
	v_add_u32_e32 v1, 0x1c78, v48
	ds_write2_b32 v1, v102, v103 offset1:1
	v_add_u32_e32 v1, 0x2080, v48
	v_mov_b32_e32 v93, v3
	s_waitcnt vmcnt(7)
	ds_write2_b32 v1, v104, v105 offset1:1
	v_add_u32_e32 v1, 0x2088, v48
	ds_write2_b32 v1, v106, v107 offset1:1
	v_add_u32_e32 v1, 0x2490, v48
	s_waitcnt vmcnt(6)
	ds_write2_b32 v1, v108, v109 offset1:1
	v_add_u32_e32 v1, 0x2498, v48
	ds_write2_b32 v1, v110, v111 offset1:1
	v_add_u32_e32 v1, 0x28a0, v48
	s_waitcnt vmcnt(5)
	ds_write2_b32 v1, v112, v113 offset1:1
	v_add_u32_e32 v1, 0x28a8, v48
	ds_write2_b32 v1, v114, v115 offset1:1
	v_add_u32_e32 v1, 0x2cb0, v48
	s_waitcnt vmcnt(4)
	ds_write2_b32 v1, v116, v117 offset1:1
	v_add_u32_e32 v1, 0x2cb8, v48
	ds_write2_b32 v1, v118, v119 offset1:1
	v_add_u32_e32 v1, 0x30c0, v48
	s_waitcnt vmcnt(3)
	ds_write2_b32 v1, v120, v121 offset1:1
	v_add_u32_e32 v1, 0x30c8, v48
	ds_write2_b32 v1, v122, v123 offset1:1
	v_add_u32_e32 v1, 0x34d0, v48
	s_waitcnt vmcnt(2)
	ds_write2_b32 v1, v124, v125 offset1:1
	v_add_u32_e32 v1, 0x34d8, v48
	ds_write2_b32 v1, v126, v127 offset1:1
	v_add_u32_e32 v1, 0x38e0, v48
	s_waitcnt vmcnt(1)
	ds_write2_b32 v1, v128, v129 offset1:1
	v_add_u32_e32 v1, 0x38e8, v48
	ds_write2_b32 v1, v130, v131 offset1:1
	v_add_u32_e32 v1, 0x3cf0, v48
	s_waitcnt vmcnt(0)
	ds_write2_b32 v1, v132, v133 offset1:1
	v_add_u32_e32 v1, 0x3cf8, v48
	ds_write2_b32 v1, v134, v135 offset1:1
	s_waitcnt lgkmcnt(0)
	ds_read2_b32 v[42:43], v49 offset0:65 offset1:73
	ds_read2_b32 v[76:77], v49 offset0:130 offset1:138
	ds_read2_b32 v[78:79], v49 offset0:195 offset1:203
	v_add_u32_e32 v1, 0x400, v49
	ds_read2_b32 v[80:81], v49 offset1:8
	ds_read2_b32 v[82:83], v1 offset0:4 offset1:12
	ds_read2_b32 v[84:85], v1 offset0:69 offset1:77
	ds_read2_b32 v[86:87], v1 offset0:134 offset1:142
	ds_read2_b32 v[88:89], v1 offset0:199 offset1:207
	s_waitcnt lgkmcnt(4)
	v_mul_f32_e32 v40, 0x41800000, v80
	v_mul_f32_e32 v41, 0x41800000, v42
	v_med3_f32 v40, v40, s87, v74
	v_med3_f32 v41, v41, s87, v74
	v_cvt_pk_fp8_f32 v90, v40, v41
	v_mul_f32_e32 v42, 0x41800000, v76
	v_mul_f32_e32 v75, 0x41800000, v78
	v_med3_f32 v42, v42, s87, v74
	v_med3_f32 v75, v75, s87, v74
	v_cvt_pk_fp8_f32 v90, v42, v75 op_sel:[0,0,1]
	v_mul_f32_e32 v42, 0x41800000, v81
	s_waitcnt lgkmcnt(3)
	v_mul_f32_e32 v76, 0x41800000, v82
	s_waitcnt lgkmcnt(2)
	v_mul_f32_e32 v78, 0x41800000, v84
	v_med3_f32 v75, v42, s87, v74
	v_mul_f32_e32 v42, 0x41800000, v43
	v_med3_f32 v76, v76, s87, v74
	v_med3_f32 v78, v78, s87, v74
	v_med3_f32 v43, v42, s87, v74
	v_mul_f32_e32 v42, 0x41800000, v77
	v_cvt_pk_fp8_f32 v91, v76, v78
	v_med3_f32 v76, v42, s87, v74
	v_mul_f32_e32 v42, 0x41800000, v79
	v_med3_f32 v77, v42, s87, v74
	v_mul_f32_e32 v42, 0x41800000, v83
	s_waitcnt lgkmcnt(1)
	v_mul_f32_e32 v80, 0x41800000, v86
	s_waitcnt lgkmcnt(0)
	v_mul_f32_e32 v40, 0x41800000, v88
	v_med3_f32 v78, v42, s87, v74
	v_mul_f32_e32 v42, 0x41800000, v85
	v_med3_f32 v80, v80, s87, v74
	v_med3_f32 v40, v40, s87, v74
	v_med3_f32 v79, v42, s87, v74
	v_mul_f32_e32 v42, 0x41800000, v87
	v_cvt_pk_fp8_f32 v91, v80, v40 op_sel:[0,0,1]
	v_med3_f32 v80, v42, s87, v74
	v_mov_b32_e32 v42, v3
	v_cvt_pk_fp8_f32 v42, v75, v43
	v_mov_b32_e32 v43, v3
	v_cvt_pk_fp8_f32 v43, v78, v79
	v_lshl_add_u64 v[40:41], s[2:3], 0, v[12:13]
	v_mul_f32_e32 v75, 0x41800000, v89
	global_store_dwordx2 v[40:41], v[90:91], off
	v_med3_f32 v75, v75, s87, v74
	v_cvt_pk_fp8_f32 v42, v76, v77 op_sel:[0,0,1]
	v_cvt_pk_fp8_f32 v43, v80, v75 op_sel:[0,0,1]
	ds_read2_b32 v[76:77], v49 offset0:81 offset1:89
	ds_read2_b32 v[78:79], v49 offset0:146 offset1:154
	ds_read2_b32 v[80:81], v49 offset0:211 offset1:219
	ds_read2_b32 v[82:83], v49 offset0:16 offset1:24
	ds_read2_b32 v[84:85], v1 offset0:20 offset1:28
	ds_read2_b32 v[86:87], v1 offset0:85 offset1:93
	ds_read2_b32 v[88:89], v1 offset0:150 offset1:158
	ds_read2_b32 v[90:91], v1 offset0:215 offset1:223
	s_waitcnt lgkmcnt(4)
	v_mul_f32_e32 v75, 0x41800000, v82
	v_mul_f32_e32 v76, 0x41800000, v76
	s_waitcnt lgkmcnt(3)
	v_mul_f32_e32 v82, 0x41800000, v84
	s_waitcnt lgkmcnt(2)
	v_mul_f32_e32 v84, 0x41800000, v86
	v_med3_f32 v75, v75, s87, v74
	v_med3_f32 v76, v76, s87, v74
	v_med3_f32 v82, v82, s87, v74
	v_med3_f32 v84, v84, s87, v74
	v_cvt_pk_fp8_f32 v92, v75, v76
	v_cvt_pk_fp8_f32 v93, v82, v84
	v_mul_f32_e32 v78, 0x41800000, v78
	v_mul_f32_e32 v80, 0x41800000, v80
	s_waitcnt lgkmcnt(1)
	v_mul_f32_e32 v86, 0x41800000, v88
	s_waitcnt lgkmcnt(0)
	v_mul_f32_e32 v75, 0x41800000, v90
	v_med3_f32 v78, v78, s87, v74
	v_med3_f32 v80, v80, s87, v74
	v_med3_f32 v86, v86, s87, v74
	v_med3_f32 v75, v75, s87, v74
	v_cvt_pk_fp8_f32 v92, v78, v80 op_sel:[0,0,1]
	v_cvt_pk_fp8_f32 v93, v86, v75 op_sel:[0,0,1]
	s_movk_i32 s2, 0x2000
	v_add_co_u32_e32 v94, vcc, s2, v40
	s_movk_i32 s2, 0x6000
	s_nop 0
	v_addc_co_u32_e32 v95, vcc, 0, v41, vcc
	global_store_dwordx2 v[94:95], v[42:43], off offset:-4096
	global_store_dwordx2 v[94:95], v[92:93], off
	v_mul_f32_e32 v42, 0x41800000, v83
	v_med3_f32 v43, v42, s87, v74
	v_mul_f32_e32 v42, 0x41800000, v77
	v_med3_f32 v75, v42, s87, v74
	v_mul_f32_e32 v42, 0x41800000, v79
	v_med3_f32 v76, v42, s87, v74
	v_mul_f32_e32 v42, 0x41800000, v81
	v_med3_f32 v77, v42, s87, v74
	v_mul_f32_e32 v42, 0x41800000, v85
	v_med3_f32 v78, v42, s87, v74
	v_mul_f32_e32 v42, 0x41800000, v87
	v_med3_f32 v79, v42, s87, v74
	v_mul_f32_e32 v42, 0x41800000, v89
	v_med3_f32 v80, v42, s87, v74
	v_mov_b32_e32 v42, v3
	v_cvt_pk_fp8_f32 v42, v43, v75
	v_mov_b32_e32 v43, v3
	v_cvt_pk_fp8_f32 v43, v78, v79
	v_mul_f32_e32 v75, 0x41800000, v91
	v_med3_f32 v75, v75, s87, v74
	v_cvt_pk_fp8_f32 v42, v76, v77 op_sel:[0,0,1]
	v_cvt_pk_fp8_f32 v43, v80, v75 op_sel:[0,0,1]
	ds_read2_b32 v[76:77], v49 offset0:97 offset1:105
	ds_read2_b32 v[78:79], v49 offset0:162 offset1:170
	ds_read2_b32 v[80:81], v49 offset0:227 offset1:235
	ds_read2_b32 v[82:83], v49 offset0:32 offset1:40
	ds_read2_b32 v[84:85], v1 offset0:36 offset1:44
	ds_read2_b32 v[86:87], v1 offset0:101 offset1:109
	ds_read2_b32 v[88:89], v1 offset0:166 offset1:174
	ds_read2_b32 v[90:91], v1 offset0:231 offset1:239
	s_waitcnt lgkmcnt(4)
	v_mul_f32_e32 v75, 0x41800000, v82
	v_mul_f32_e32 v76, 0x41800000, v76
	s_waitcnt lgkmcnt(3)
	v_mul_f32_e32 v82, 0x41800000, v84
	s_waitcnt lgkmcnt(2)
	v_mul_f32_e32 v84, 0x41800000, v86
	v_med3_f32 v75, v75, s87, v74
	v_med3_f32 v76, v76, s87, v74
	v_med3_f32 v82, v82, s87, v74
	v_med3_f32 v84, v84, s87, v74
	v_mov_b32_e32 v92, v3
	v_mov_b32_e32 v93, v3
	v_cvt_pk_fp8_f32 v92, v75, v76
	v_cvt_pk_fp8_f32 v93, v82, v84
	v_mul_f32_e32 v78, 0x41800000, v78
	v_mul_f32_e32 v80, 0x41800000, v80
	s_waitcnt lgkmcnt(1)
	v_mul_f32_e32 v86, 0x41800000, v88
	s_waitcnt lgkmcnt(0)
	v_mul_f32_e32 v75, 0x41800000, v90
	v_med3_f32 v78, v78, s87, v74
	v_med3_f32 v80, v80, s87, v74
	v_med3_f32 v86, v86, s87, v74
	v_med3_f32 v75, v75, s87, v74
	v_cvt_pk_fp8_f32 v92, v78, v80 op_sel:[0,0,1]
	v_cvt_pk_fp8_f32 v93, v86, v75 op_sel:[0,0,1]
	v_add_co_u32_e32 v94, vcc, s68, v40
	s_nop 1
	v_addc_co_u32_e32 v95, vcc, 0, v41, vcc
	global_store_dwordx2 v[94:95], v[42:43], off offset:-4096
	global_store_dwordx2 v[94:95], v[92:93], off
	v_mul_f32_e32 v42, 0x41800000, v83
	v_med3_f32 v43, v42, s87, v74
	v_mul_f32_e32 v42, 0x41800000, v77
	v_med3_f32 v75, v42, s87, v74
	v_mul_f32_e32 v42, 0x41800000, v79
	v_med3_f32 v76, v42, s87, v74
	v_mul_f32_e32 v42, 0x41800000, v81
	v_med3_f32 v77, v42, s87, v74
	v_mul_f32_e32 v42, 0x41800000, v85
	v_med3_f32 v78, v42, s87, v74
	v_mul_f32_e32 v42, 0x41800000, v87
	v_med3_f32 v79, v42, s87, v74
	v_mul_f32_e32 v42, 0x41800000, v89
	v_med3_f32 v80, v42, s87, v74
	v_mov_b32_e32 v42, v3
	v_cvt_pk_fp8_f32 v42, v43, v75
	v_mov_b32_e32 v43, v3
	v_cvt_pk_fp8_f32 v43, v78, v79
	v_mul_f32_e32 v75, 0x41800000, v91
	v_med3_f32 v75, v75, s87, v74
	v_cvt_pk_fp8_f32 v42, v76, v77 op_sel:[0,0,1]
	v_cvt_pk_fp8_f32 v43, v80, v75 op_sel:[0,0,1]
	ds_read2_b32 v[76:77], v49 offset0:113 offset1:121
	ds_read2_b32 v[78:79], v49 offset0:178 offset1:186
	ds_read2_b32 v[80:81], v49 offset0:243 offset1:251
	ds_read2_b32 v[82:83], v49 offset0:48 offset1:56
	ds_read2_b32 v[84:85], v1 offset0:52 offset1:60
	ds_read2_b32 v[86:87], v1 offset0:117 offset1:125
	ds_read2_b32 v[88:89], v1 offset0:182 offset1:190
	ds_read2_b32 v[90:91], v1 offset0:247 offset1:255
	s_waitcnt lgkmcnt(4)
	v_mul_f32_e32 v1, 0x41800000, v82
	v_mul_f32_e32 v75, 0x41800000, v76
	v_mul_f32_e32 v76, 0x41800000, v78
	v_mul_f32_e32 v78, 0x41800000, v80
	s_waitcnt lgkmcnt(3)
	v_mul_f32_e32 v80, 0x41800000, v84
	s_waitcnt lgkmcnt(2)
	v_mul_f32_e32 v82, 0x41800000, v86
	v_med3_f32 v1, v1, s87, v74
	v_med3_f32 v75, v75, s87, v74
	v_med3_f32 v80, v80, s87, v74
	v_med3_f32 v82, v82, s87, v74
	v_mov_b32_e32 v92, v3
	v_mov_b32_e32 v93, v3
	v_cvt_pk_fp8_f32 v92, v1, v75
	v_cvt_pk_fp8_f32 v93, v80, v82
	s_waitcnt lgkmcnt(1)
	v_mul_f32_e32 v84, 0x41800000, v88
	s_waitcnt lgkmcnt(0)
	v_mul_f32_e32 v1, 0x41800000, v90
	v_med3_f32 v76, v76, s87, v74
	v_med3_f32 v78, v78, s87, v74
	v_med3_f32 v84, v84, s87, v74
	v_med3_f32 v1, v1, s87, v74
	v_cvt_pk_fp8_f32 v92, v76, v78 op_sel:[0,0,1]
	v_cvt_pk_fp8_f32 v93, v84, v1 op_sel:[0,0,1]
	v_add_co_u32_e32 v94, vcc, s2, v40
	v_mul_f32_e32 v1, 0x41800000, v83
	s_nop 0
	v_addc_co_u32_e32 v95, vcc, 0, v41, vcc
	global_store_dwordx2 v[94:95], v[42:43], off offset:-4096
	global_store_dwordx2 v[94:95], v[92:93], off
	v_mul_f32_e32 v42, 0x41800000, v77
	v_med3_f32 v43, v42, s87, v74
	v_mul_f32_e32 v42, 0x41800000, v79
	v_med3_f32 v75, v42, s87, v74
	v_mul_f32_e32 v42, 0x41800000, v81
	v_med3_f32 v76, v42, s87, v74
	v_mul_f32_e32 v42, 0x41800000, v85
	v_med3_f32 v77, v42, s87, v74
	v_mul_f32_e32 v42, 0x41800000, v87
	v_med3_f32 v78, v42, s87, v74
	v_mul_f32_e32 v42, 0x41800000, v89
	v_med3_f32 v1, v1, s87, v74
	v_med3_f32 v79, v42, s87, v74
	v_mov_b32_e32 v42, v3
	v_cvt_pk_fp8_f32 v42, v1, v43
	v_mov_b32_e32 v43, v3
	v_cvt_pk_fp8_f32 v43, v77, v78
	v_mul_f32_e32 v1, 0x41800000, v91
	v_med3_f32 v1, v1, s87, v74
	v_cvt_pk_fp8_f32 v42, v75, v76 op_sel:[0,0,1]
	v_cvt_pk_fp8_f32 v43, v79, v1 op_sel:[0,0,1]
	v_add_co_u32_e32 v40, vcc, 0x7000, v40
	s_nop 1
	v_addc_co_u32_e32 v41, vcc, 0, v41, vcc
	global_store_dwordx2 v[40:41], v[42:43], off
	s_waitcnt lgkmcnt(0)

.LBB0_257:
	s_andn2_b64 vcc, exec, s[2:3]
	s_cbranch_vccnz .LBB0_259
	s_cmpk_gt_u32 s75, 0x1aff
	s_cselect_b64 s[2:3], -1, 0
	s_and_b64 s[4:5], s[2:3], exec
	s_movk_i32 s4, 0xe500
	s_cselect_b32 s4, s4, 0xffffe600
	s_add_i32 s8, s4, s75
	s_lshl_b32 s9, s8, 6
	s_and_b64 s[4:5], s[2:3], exec
	s_cselect_b32 s10, s45, s43
	s_cselect_b32 s11, s44, s42
	s_lshl_b32 s4, s8, 3
	s_and_b32 s34, s4, 0x7fffffc0
	s_lshl_b64 s[4:5], s[34:35], 11
	s_add_u32 s4, s11, s4
	s_addc_u32 s5, s10, s5
	s_lshl_b32 s10, s8, 8
	s_and_b32 s10, s10, 0x700
	s_add_u32 s4, s4, s10
	s_addc_u32 s5, s5, 0
	v_lshl_add_u64 v[132:133], s[4:5], 0, v[14:15]
	s_movk_i32 s4, 0x2000
	v_add_co_u32_e32 v76, vcc, s4, v132
	s_movk_i32 s4, 0x6000
	s_nop 0
	v_addc_co_u32_e32 v77, vcc, 0, v133, vcc
	v_add_co_u32_e32 v80, vcc, s68, v132
	global_load_dwordx4 v[40:43], v[132:133], off nt
	s_nop 0
	global_load_dwordx4 v[76:79], v[76:77], off nt
	v_addc_co_u32_e32 v81, vcc, 0, v133, vcc
	v_add_co_u32_e32 v84, vcc, s4, v132
	s_mov_b32 s4, 0xa000
	s_nop 0
	v_addc_co_u32_e32 v85, vcc, 0, v133, vcc
	global_load_dwordx4 v[80:83], v[80:81], off nt
	s_nop 0
	global_load_dwordx4 v[84:87], v[84:85], off nt
	v_add_co_u32_e32 v88, vcc, s88, v132
	v_add_u32_e32 v1, 0x410, v48
	s_nop 0
	v_addc_co_u32_e32 v89, vcc, 0, v133, vcc
	v_add_co_u32_e32 v92, vcc, s4, v132
	s_mov_b32 s4, 0xe000
	s_nop 0
	v_addc_co_u32_e32 v93, vcc, 0, v133, vcc
	global_load_dwordx4 v[88:91], v[88:89], off nt
	s_nop 0
	global_load_dwordx4 v[92:95], v[92:93], off nt
	v_add_co_u32_e32 v96, vcc, s92, v132
	s_nop 1
	v_addc_co_u32_e32 v97, vcc, 0, v133, vcc
	v_add_co_u32_e32 v100, vcc, s4, v132
	s_mov_b32 s4, 0x12000
	s_nop 0
	v_addc_co_u32_e32 v101, vcc, 0, v133, vcc
	global_load_dwordx4 v[96:99], v[96:97], off nt
	s_nop 0
	global_load_dwordx4 v[100:103], v[100:101], off nt
	v_add_co_u32_e32 v104, vcc, s89, v132
	s_nop 1
	v_addc_co_u32_e32 v105, vcc, 0, v133, vcc
	v_add_co_u32_e32 v108, vcc, s4, v132
	s_mov_b32 s4, 0x16000
	s_nop 0
	v_addc_co_u32_e32 v109, vcc, 0, v133, vcc
	global_load_dwordx4 v[104:107], v[104:105], off nt
	s_nop 0
	global_load_dwordx4 v[108:111], v[108:109], off nt
	v_add_co_u32_e32 v112, vcc, s93, v132
	s_nop 1
	v_addc_co_u32_e32 v113, vcc, 0, v133, vcc
	v_add_co_u32_e32 v116, vcc, s4, v132
	s_mov_b32 s4, 0x1a000
	s_nop 0
	v_addc_co_u32_e32 v117, vcc, 0, v133, vcc
	global_load_dwordx4 v[112:115], v[112:113], off nt
	s_nop 0
	global_load_dwordx4 v[116:119], v[116:117], off nt
	v_add_co_u32_e32 v120, vcc, s90, v132
	s_nop 1
	v_addc_co_u32_e32 v121, vcc, 0, v133, vcc
	v_add_co_u32_e32 v124, vcc, s4, v132
	s_mov_b32 s4, 0x1c000
	s_nop 0
	v_addc_co_u32_e32 v125, vcc, 0, v133, vcc
	global_load_dwordx4 v[120:123], v[120:121], off nt
	s_nop 0
	global_load_dwordx4 v[124:127], v[124:125], off nt
	v_add_co_u32_e32 v128, vcc, s4, v132
	s_mov_b32 s4, 0x1e000
	s_nop 0
	v_addc_co_u32_e32 v129, vcc, 0, v133, vcc
	global_load_dwordx4 v[128:131], v[128:129], off nt
	v_add_co_u32_e32 v132, vcc, s4, v132
	s_lshl_b32 s4, s8, 7
	s_nop 0
	v_addc_co_u32_e32 v133, vcc, 0, v133, vcc
	global_load_dwordx4 v[132:135], v[132:133], off nt
	s_waitcnt vmcnt(15)
	ds_write2_b32 v48, v40, v41 offset1:1
	ds_write2_b32 v48, v42, v43 offset0:2 offset1:3
	s_waitcnt vmcnt(14)
	ds_write2_b32 v1, v76, v77 offset1:1
	v_add_u32_e32 v1, 0x418, v48
	ds_write2_b32 v1, v78, v79 offset1:1
	v_add_u32_e32 v1, 0x820, v48
	s_and_b32 s4, s4, 0x300
	s_and_b64 s[2:3], s[2:3], exec
	s_cselect_b32 s2, 0x80, 0
	s_waitcnt vmcnt(13)
	ds_write2_b32 v1, v80, v81 offset1:1
	v_add_u32_e32 v1, 0x828, v48
	ds_write2_b32 v1, v82, v83 offset1:1
	v_add_u32_e32 v1, 0xc30, v48
	s_waitcnt vmcnt(12)
	ds_write2_b32 v1, v84, v85 offset1:1
	v_add_u32_e32 v1, 0xc38, v48
	ds_write2_b32 v1, v86, v87 offset1:1
	v_add_u32_e32 v1, 0x1040, v48
	s_or_b32 s2, s4, s2
	s_and_b32 s3, s9, 64
	s_or_b32 s2, s2, s3
	s_waitcnt vmcnt(11)
	ds_write2_b32 v1, v88, v89 offset1:1
	v_add_u32_e32 v1, 0x1048, v48
	ds_write2_b32 v1, v90, v91 offset1:1
	v_add_u32_e32 v1, 0x1450, v48
	s_waitcnt vmcnt(10)
	ds_write2_b32 v1, v92, v93 offset1:1
	v_add_u32_e32 v1, 0x1458, v48
	ds_write2_b32 v1, v94, v95 offset1:1
	v_add_u32_e32 v1, 0x1860, v48
	v_mov_b32_e32 v90, v3
	v_mov_b32_e32 v91, v3
	s_lshl_b32 s2, s2, 11
	s_waitcnt vmcnt(9)
	ds_write2_b32 v1, v96, v97 offset1:1
	v_add_u32_e32 v1, 0x1868, v48
	ds_write2_b32 v1, v98, v99 offset1:1
	v_add_u32_e32 v1, 0x1c70, v48
	s_waitcnt vmcnt(8)
	ds_write2_b32 v1, v100, v101 offset1:1
	v_add_u32_e32 v1, 0x1c78, v48
	ds_write2_b32 v1, v102, v103 offset1:1
	v_add_u32_e32 v1, 0x2080, v48
	s_bitset1_b32 s2, 27
	v_readlane_b32 s3, v255, 15
	s_add_u32 s2, s3, s2
	s_waitcnt vmcnt(7)
	ds_write2_b32 v1, v104, v105 offset1:1
	v_add_u32_e32 v1, 0x2088, v48
	ds_write2_b32 v1, v106, v107 offset1:1
	v_add_u32_e32 v1, 0x2490, v48
	s_waitcnt vmcnt(6)
	ds_write2_b32 v1, v108, v109 offset1:1
	v_add_u32_e32 v1, 0x2498, v48
	ds_write2_b32 v1, v110, v111 offset1:1
	v_add_u32_e32 v1, 0x28a0, v48
	v_readlane_b32 s3, v255, 17
	s_addc_u32 s3, s3, 0
	s_add_u32 s2, s2, s34
	s_waitcnt vmcnt(5)
	ds_write2_b32 v1, v112, v113 offset1:1
	v_add_u32_e32 v1, 0x28a8, v48
	ds_write2_b32 v1, v114, v115 offset1:1
	v_add_u32_e32 v1, 0x2cb0, v48
	s_waitcnt vmcnt(4)
	ds_write2_b32 v1, v116, v117 offset1:1
	v_add_u32_e32 v1, 0x2cb8, v48
	ds_write2_b32 v1, v118, v119 offset1:1
	v_add_u32_e32 v1, 0x30c0, v48
	s_addc_u32 s3, s3, 0
	s_waitcnt vmcnt(3)
	ds_write2_b32 v1, v120, v121 offset1:1
	v_add_u32_e32 v1, 0x30c8, v48
	ds_write2_b32 v1, v122, v123 offset1:1
	v_add_u32_e32 v1, 0x34d0, v48
	s_waitcnt vmcnt(2)
	ds_write2_b32 v1, v124, v125 offset1:1
	v_add_u32_e32 v1, 0x34d8, v48
	ds_write2_b32 v1, v126, v127 offset1:1
	v_add_u32_e32 v1, 0x38e0, v48
	s_waitcnt vmcnt(1)
	ds_write2_b32 v1, v128, v129 offset1:1
	v_add_u32_e32 v1, 0x38e8, v48
	ds_write2_b32 v1, v130, v131 offset1:1
	v_add_u32_e32 v1, 0x3cf0, v48
	s_waitcnt vmcnt(0)
	ds_write2_b32 v1, v132, v133 offset1:1
	v_add_u32_e32 v1, 0x3cf8, v48
	ds_write2_b32 v1, v134, v135 offset1:1
	s_waitcnt lgkmcnt(0)
	ds_read2_b32 v[42:43], v49 offset0:65 offset1:73
	ds_read2_b32 v[76:77], v49 offset0:130 offset1:138
	ds_read2_b32 v[78:79], v49 offset0:195 offset1:203
	v_add_u32_e32 v1, 0x400, v49
	ds_read2_b32 v[80:81], v49 offset1:8
	ds_read2_b32 v[82:83], v1 offset0:4 offset1:12
	ds_read2_b32 v[84:85], v1 offset0:69 offset1:77
	ds_read2_b32 v[86:87], v1 offset0:134 offset1:142
	ds_read2_b32 v[88:89], v1 offset0:199 offset1:207
	s_waitcnt lgkmcnt(4)
	v_mul_f32_e32 v40, 0x41800000, v80
	v_mul_f32_e32 v41, 0x41800000, v42
	v_med3_f32 v40, v40, s87, v74
	v_med3_f32 v41, v41, s87, v74
	v_cvt_pk_fp8_f32 v90, v40, v41
	v_mul_f32_e32 v42, 0x41800000, v76
	v_mul_f32_e32 v75, 0x41800000, v78
	v_med3_f32 v42, v42, s87, v74
	v_med3_f32 v75, v75, s87, v74
	v_cvt_pk_fp8_f32 v90, v42, v75 op_sel:[0,0,1]
	v_mul_f32_e32 v42, 0x41800000, v81
	s_waitcnt lgkmcnt(3)
	v_mul_f32_e32 v76, 0x41800000, v82
	s_waitcnt lgkmcnt(2)
	v_mul_f32_e32 v78, 0x41800000, v84
	v_med3_f32 v75, v42, s87, v74
	v_mul_f32_e32 v42, 0x41800000, v43
	v_med3_f32 v76, v76, s87, v74
	v_med3_f32 v78, v78, s87, v74
	v_med3_f32 v43, v42, s87, v74
	v_mul_f32_e32 v42, 0x41800000, v77
	v_cvt_pk_fp8_f32 v91, v76, v78
	v_med3_f32 v76, v42, s87, v74
	v_mul_f32_e32 v42, 0x41800000, v79
	v_med3_f32 v77, v42, s87, v74
	v_mul_f32_e32 v42, 0x41800000, v83
	s_waitcnt lgkmcnt(1)
	v_mul_f32_e32 v80, 0x41800000, v86
	s_waitcnt lgkmcnt(0)
	v_mul_f32_e32 v40, 0x41800000, v88
	v_med3_f32 v78, v42, s87, v74
	v_mul_f32_e32 v42, 0x41800000, v85
	v_med3_f32 v80, v80, s87, v74
	v_med3_f32 v40, v40, s87, v74
	v_med3_f32 v79, v42, s87, v74
	v_mul_f32_e32 v42, 0x41800000, v87
	v_cvt_pk_fp8_f32 v91, v80, v40 op_sel:[0,0,1]
	v_med3_f32 v80, v42, s87, v74
	v_mov_b32_e32 v42, v3
	v_cvt_pk_fp8_f32 v42, v75, v43
	v_mov_b32_e32 v43, v3
	v_cvt_pk_fp8_f32 v43, v78, v79
	v_mul_f32_e32 v75, 0x41800000, v89
	v_med3_f32 v75, v75, s87, v74
	v_cvt_pk_fp8_f32 v42, v76, v77 op_sel:[0,0,1]
	v_cvt_pk_fp8_f32 v43, v80, v75 op_sel:[0,0,1]
	v_lshl_add_u64 v[40:41], s[2:3], 0, v[16:17]
	v_add_co_u32_e32 v76, vcc, s68, v40
	global_store_dwordx2 v[40:41], v[90:91], off
	s_nop 0
	v_addc_co_u32_e32 v77, vcc, 0, v41, vcc
	global_store_dwordx2 v[76:77], v[42:43], off
	ds_read2_b32 v[42:43], v49 offset0:81 offset1:89
	ds_read2_b32 v[76:77], v49 offset0:146 offset1:154
	ds_read2_b32 v[78:79], v49 offset0:211 offset1:219
	ds_read2_b32 v[80:81], v49 offset0:16 offset1:24
	ds_read2_b32 v[82:83], v1 offset0:20 offset1:28
	ds_read2_b32 v[84:85], v1 offset0:85 offset1:93
	ds_read2_b32 v[86:87], v1 offset0:150 offset1:158
	ds_read2_b32 v[88:89], v1 offset0:215 offset1:223
	s_waitcnt lgkmcnt(4)
	v_mul_f32_e32 v75, 0x41800000, v80
	s_waitcnt lgkmcnt(3)
	v_mul_f32_e32 v80, 0x41800000, v82
	s_waitcnt lgkmcnt(2)
	v_mul_f32_e32 v82, 0x41800000, v84
	v_med3_f32 v80, v80, s87, v74
	v_med3_f32 v82, v82, s87, v74
	v_mov_b32_e32 v91, v3
	v_mul_f32_e32 v42, 0x41800000, v42
	v_cvt_pk_fp8_f32 v91, v80, v82
	v_med3_f32 v75, v75, s87, v74
	v_med3_f32 v42, v42, s87, v74
	v_mov_b32_e32 v90, v3
	s_waitcnt lgkmcnt(1)
	v_mul_f32_e32 v84, 0x41800000, v86
	v_cvt_pk_fp8_f32 v90, v75, v42
	s_waitcnt lgkmcnt(0)
	v_mul_f32_e32 v42, 0x41800000, v88
	v_med3_f32 v84, v84, s87, v74
	v_med3_f32 v42, v42, s87, v74
	v_cvt_pk_fp8_f32 v91, v84, v42 op_sel:[0,0,1]
	v_mul_f32_e32 v42, 0x41800000, v81
	v_mul_f32_e32 v76, 0x41800000, v76
	v_mul_f32_e32 v78, 0x41800000, v78
	v_med3_f32 v75, v42, s87, v74
	v_mul_f32_e32 v42, 0x41800000, v43
	v_med3_f32 v76, v76, s87, v74
	v_med3_f32 v78, v78, s87, v74
	v_med3_f32 v43, v42, s87, v74
	v_mul_f32_e32 v42, 0x41800000, v77
	v_cvt_pk_fp8_f32 v90, v76, v78 op_sel:[0,0,1]
	v_med3_f32 v76, v42, s87, v74
	v_mul_f32_e32 v42, 0x41800000, v79
	v_med3_f32 v77, v42, s87, v74
	v_mul_f32_e32 v42, 0x41800000, v83
	v_med3_f32 v78, v42, s87, v74
	v_mul_f32_e32 v42, 0x41800000, v85
	v_med3_f32 v79, v42, s87, v74
	v_mul_f32_e32 v42, 0x41800000, v87
	v_med3_f32 v80, v42, s87, v74
	v_mov_b32_e32 v42, v3
	v_cvt_pk_fp8_f32 v42, v75, v43
	v_mov_b32_e32 v43, v3
	v_cvt_pk_fp8_f32 v43, v78, v79
	v_mul_f32_e32 v75, 0x41800000, v89
	v_med3_f32 v75, v75, s87, v74
	v_add_co_u32_e32 v92, vcc, s88, v40
	v_cvt_pk_fp8_f32 v42, v76, v77 op_sel:[0,0,1]
	v_cvt_pk_fp8_f32 v43, v80, v75 op_sel:[0,0,1]
	v_addc_co_u32_e32 v93, vcc, 0, v41, vcc
	v_add_co_u32_e32 v76, vcc, s92, v40
	global_store_dwordx2 v[92:93], v[90:91], off
	s_nop 0
	v_addc_co_u32_e32 v77, vcc, 0, v41, vcc
	global_store_dwordx2 v[76:77], v[42:43], off
	ds_read2_b32 v[42:43], v49 offset0:97 offset1:105
	ds_read2_b32 v[76:77], v49 offset0:162 offset1:170
	ds_read2_b32 v[78:79], v49 offset0:227 offset1:235
	ds_read2_b32 v[80:81], v49 offset0:32 offset1:40
	ds_read2_b32 v[82:83], v1 offset0:36 offset1:44
	ds_read2_b32 v[84:85], v1 offset0:101 offset1:109
	ds_read2_b32 v[86:87], v1 offset0:166 offset1:174
	ds_read2_b32 v[88:89], v1 offset0:231 offset1:239
	s_waitcnt lgkmcnt(4)
	v_mul_f32_e32 v75, 0x41800000, v80
	s_waitcnt lgkmcnt(3)
	v_mul_f32_e32 v80, 0x41800000, v82
	s_waitcnt lgkmcnt(2)
	v_mul_f32_e32 v82, 0x41800000, v84
	v_med3_f32 v80, v80, s87, v74
	v_med3_f32 v82, v82, s87, v74
	v_mov_b32_e32 v91, v3
	v_mul_f32_e32 v42, 0x41800000, v42
	v_cvt_pk_fp8_f32 v91, v80, v82
	v_med3_f32 v75, v75, s87, v74
	v_med3_f32 v42, v42, s87, v74
	v_mov_b32_e32 v90, v3
	s_waitcnt lgkmcnt(1)
	v_mul_f32_e32 v84, 0x41800000, v86
	v_cvt_pk_fp8_f32 v90, v75, v42
	s_waitcnt lgkmcnt(0)
	v_mul_f32_e32 v42, 0x41800000, v88
	v_med3_f32 v84, v84, s87, v74
	v_med3_f32 v42, v42, s87, v74
	v_cvt_pk_fp8_f32 v91, v84, v42 op_sel:[0,0,1]
	v_mul_f32_e32 v42, 0x41800000, v81
	v_mul_f32_e32 v76, 0x41800000, v76
	v_mul_f32_e32 v78, 0x41800000, v78
	v_med3_f32 v75, v42, s87, v74
	v_mul_f32_e32 v42, 0x41800000, v43
	v_med3_f32 v76, v76, s87, v74
	v_med3_f32 v78, v78, s87, v74
	v_med3_f32 v43, v42, s87, v74
	v_mul_f32_e32 v42, 0x41800000, v77
	v_cvt_pk_fp8_f32 v90, v76, v78 op_sel:[0,0,1]
	v_med3_f32 v76, v42, s87, v74
	v_mul_f32_e32 v42, 0x41800000, v79
	v_med3_f32 v77, v42, s87, v74
	v_mul_f32_e32 v42, 0x41800000, v83
	v_med3_f32 v78, v42, s87, v74
	v_mul_f32_e32 v42, 0x41800000, v85
	v_med3_f32 v79, v42, s87, v74
	v_mul_f32_e32 v42, 0x41800000, v87
	v_med3_f32 v80, v42, s87, v74
	v_mov_b32_e32 v42, v3
	v_cvt_pk_fp8_f32 v42, v75, v43
	v_mov_b32_e32 v43, v3
	v_cvt_pk_fp8_f32 v43, v78, v79
	v_mul_f32_e32 v75, 0x41800000, v89
	v_med3_f32 v75, v75, s87, v74
	v_add_co_u32_e32 v92, vcc, s89, v40
	v_cvt_pk_fp8_f32 v42, v76, v77 op_sel:[0,0,1]
	v_cvt_pk_fp8_f32 v43, v80, v75 op_sel:[0,0,1]
	v_addc_co_u32_e32 v93, vcc, 0, v41, vcc
	v_add_co_u32_e32 v76, vcc, s93, v40
	global_store_dwordx2 v[92:93], v[90:91], off
	s_nop 0
	v_addc_co_u32_e32 v77, vcc, 0, v41, vcc
	global_store_dwordx2 v[76:77], v[42:43], off
	ds_read2_b32 v[42:43], v49 offset0:113 offset1:121
	ds_read2_b32 v[76:77], v49 offset0:178 offset1:186
	ds_read2_b32 v[78:79], v49 offset0:243 offset1:251
	ds_read2_b32 v[80:81], v49 offset0:48 offset1:56
	ds_read2_b32 v[82:83], v1 offset0:52 offset1:60
	ds_read2_b32 v[84:85], v1 offset0:117 offset1:125
	ds_read2_b32 v[86:87], v1 offset0:182 offset1:190
	ds_read2_b32 v[88:89], v1 offset0:247 offset1:255
	s_waitcnt lgkmcnt(4)
	v_mul_f32_e32 v1, 0x41800000, v80
	v_mul_f32_e32 v42, 0x41800000, v42
	v_med3_f32 v1, v1, s87, v74
	v_med3_f32 v42, v42, s87, v74
	v_mov_b32_e32 v90, v3
	v_cvt_pk_fp8_f32 v90, v1, v42
	v_mul_f32_e32 v75, 0x41800000, v76
	v_mul_f32_e32 v76, 0x41800000, v78
	s_waitcnt lgkmcnt(3)
	v_mul_f32_e32 v78, 0x41800000, v82
	s_waitcnt lgkmcnt(2)
	v_mul_f32_e32 v80, 0x41800000, v84
	v_med3_f32 v78, v78, s87, v74
	v_med3_f32 v80, v80, s87, v74
	v_mov_b32_e32 v91, v3
	v_mul_f32_e32 v42, 0x41800000, v43
	v_med3_f32 v75, v75, s87, v74
	v_med3_f32 v76, v76, s87, v74
	v_cvt_pk_fp8_f32 v91, v78, v80
	v_med3_f32 v43, v42, s87, v74
	v_mul_f32_e32 v42, 0x41800000, v77
	v_cvt_pk_fp8_f32 v90, v75, v76 op_sel:[0,0,1]
	v_med3_f32 v75, v42, s87, v74
	v_mul_f32_e32 v42, 0x41800000, v79
	s_waitcnt lgkmcnt(1)
	v_mul_f32_e32 v82, 0x41800000, v86
	s_waitcnt lgkmcnt(0)
	v_mul_f32_e32 v1, 0x41800000, v88
	v_med3_f32 v76, v42, s87, v74
	v_mul_f32_e32 v42, 0x41800000, v83
	v_med3_f32 v82, v82, s87, v74
	v_med3_f32 v1, v1, s87, v74
	v_med3_f32 v77, v42, s87, v74
	v_mul_f32_e32 v42, 0x41800000, v85
	v_cvt_pk_fp8_f32 v91, v82, v1 op_sel:[0,0,1]
	v_mul_f32_e32 v1, 0x41800000, v81
	v_med3_f32 v78, v42, s87, v74
	v_mul_f32_e32 v42, 0x41800000, v87
	v_med3_f32 v1, v1, s87, v74
	v_med3_f32 v79, v42, s87, v74
	v_mov_b32_e32 v42, v3
	v_cvt_pk_fp8_f32 v42, v1, v43
	v_mov_b32_e32 v43, v3
	v_cvt_pk_fp8_f32 v43, v77, v78
	v_mul_f32_e32 v1, 0x41800000, v89
	v_med3_f32 v1, v1, s87, v74
	v_add_co_u32_e32 v92, vcc, s90, v40
	v_cvt_pk_fp8_f32 v42, v75, v76 op_sel:[0,0,1]
	v_cvt_pk_fp8_f32 v43, v79, v1 op_sel:[0,0,1]
	v_addc_co_u32_e32 v93, vcc, 0, v41, vcc
	v_add_co_u32_e32 v40, vcc, 0x1c000, v40
	global_store_dwordx2 v[92:93], v[90:91], off
	s_nop 0
	v_addc_co_u32_e32 v41, vcc, 0, v41, vcc
	global_store_dwordx2 v[40:41], v[42:43], off
	s_waitcnt lgkmcnt(0)

.LBB0_260:
	s_andn2_b64 vcc, exec, s[2:3]
	s_cbranch_vccnz .LBB0_262
	s_and_b32 s2, s80, 0x3fc0
	s_add_i32 s34, s2, 0xffffd400
	s_lshl_b64 s[2:3], s[34:35], 13
	s_add_u32 s2, s60, s2
	s_addc_u32 s3, s61, s3
	s_and_b32 s4, s95, 0x7c0
	s_lshl_b32 s5, s4, 2
	s_add_u32 s2, s2, s5
	s_addc_u32 s3, s3, 0
	v_lshl_add_u64 v[132:133], s[2:3], 0, v[10:11]
	v_add_co_u32_e32 v76, vcc, s88, v132
	s_mov_b32 s2, 0x28000
	s_nop 0
	v_addc_co_u32_e32 v77, vcc, 0, v133, vcc
	v_add_co_u32_e32 v80, vcc, s89, v132
	global_load_dwordx4 v[40:43], v[132:133], off nt
	s_nop 0
	global_load_dwordx4 v[76:79], v[76:77], off nt
	v_addc_co_u32_e32 v81, vcc, 0, v133, vcc
	v_add_co_u32_e32 v84, vcc, s90, v132
	v_add_u32_e32 v1, 0x410, v48
	s_nop 0
	v_addc_co_u32_e32 v85, vcc, 0, v133, vcc
	global_load_dwordx4 v[80:83], v[80:81], off nt
	s_nop 0
	global_load_dwordx4 v[84:87], v[84:85], off nt
	v_add_co_u32_e32 v88, vcc, s91, v132
	v_readlane_b32 s3, v255, 11
	s_nop 0
	v_addc_co_u32_e32 v89, vcc, 0, v133, vcc
	v_add_co_u32_e32 v92, vcc, s2, v132
	s_mov_b32 s2, 0x30000
	s_nop 0
	v_addc_co_u32_e32 v93, vcc, 0, v133, vcc
	global_load_dwordx4 v[88:91], v[88:89], off nt
	s_nop 0
	global_load_dwordx4 v[92:95], v[92:93], off nt
	v_add_co_u32_e32 v96, vcc, s2, v132
	s_lshl_b32 s2, s4, 11
	s_nop 0
	v_addc_co_u32_e32 v97, vcc, 0, v133, vcc
	v_add_co_u32_e32 v100, vcc, s94, v132
	s_add_u32 s2, s3, s2
	s_nop 0
	v_addc_co_u32_e32 v101, vcc, 0, v133, vcc
	global_load_dwordx4 v[96:99], v[96:97], off nt
	s_nop 0
	global_load_dwordx4 v[100:103], v[100:101], off nt
	v_add_co_u32_e32 v104, vcc, s1, v132
	v_readlane_b32 s3, v255, 13
	s_nop 0
	v_addc_co_u32_e32 v105, vcc, 0, v133, vcc
	v_add_co_u32_e32 v108, vcc, s0, v132
	s_addc_u32 s3, s3, 0
	s_nop 0
	v_addc_co_u32_e32 v109, vcc, 0, v133, vcc
	global_load_dwordx4 v[104:107], v[104:105], off nt
	s_nop 0
	global_load_dwordx4 v[108:111], v[108:109], off nt
	v_add_co_u32_e32 v112, vcc, s78, v132
	s_add_u32 s2, s2, s34
	s_nop 0
	v_addc_co_u32_e32 v113, vcc, 0, v133, vcc
	v_add_co_u32_e32 v116, vcc, s79, v132
	s_addc_u32 s3, s3, 0
	s_nop 0
	v_addc_co_u32_e32 v117, vcc, 0, v133, vcc
	global_load_dwordx4 v[112:115], v[112:113], off nt
	s_nop 0
	global_load_dwordx4 v[116:119], v[116:117], off nt
	v_add_co_u32_e32 v120, vcc, s30, v132
	s_nop 1
	v_addc_co_u32_e32 v121, vcc, 0, v133, vcc
	global_load_dwordx4 v[120:123], v[120:121], off nt
	v_add_co_u32_e32 v124, vcc, s31, v132
	s_nop 1
	v_addc_co_u32_e32 v125, vcc, 0, v133, vcc
	global_load_dwordx4 v[124:127], v[124:125], off nt
	v_add_co_u32_e32 v128, vcc, s73, v132
	s_nop 1
	v_addc_co_u32_e32 v129, vcc, 0, v133, vcc
	global_load_dwordx4 v[128:131], v[128:129], off nt
	v_add_co_u32_e32 v132, vcc, s77, v132
	s_nop 1
	v_addc_co_u32_e32 v133, vcc, 0, v133, vcc
	global_load_dwordx4 v[132:135], v[132:133], off nt
	s_waitcnt vmcnt(15)
	ds_write2_b32 v48, v40, v41 offset1:1
	ds_write2_b32 v48, v42, v43 offset0:2 offset1:3
	s_waitcnt vmcnt(14)
	ds_write2_b32 v1, v76, v77 offset1:1
	v_add_u32_e32 v1, 0x418, v48
	ds_write2_b32 v1, v78, v79 offset1:1
	v_add_u32_e32 v1, 0x820, v48
	s_waitcnt vmcnt(13)
	ds_write2_b32 v1, v80, v81 offset1:1
	v_add_u32_e32 v1, 0x828, v48
	ds_write2_b32 v1, v82, v83 offset1:1
	v_add_u32_e32 v1, 0xc30, v48
	s_waitcnt vmcnt(12)
	ds_write2_b32 v1, v84, v85 offset1:1
	v_add_u32_e32 v1, 0xc38, v48
	ds_write2_b32 v1, v86, v87 offset1:1
	v_add_u32_e32 v1, 0x1040, v48
	s_waitcnt vmcnt(11)
	ds_write2_b32 v1, v88, v89 offset1:1
	v_add_u32_e32 v1, 0x1048, v48
	ds_write2_b32 v1, v90, v91 offset1:1
	v_add_u32_e32 v1, 0x1450, v48
	s_waitcnt vmcnt(10)
	ds_write2_b32 v1, v92, v93 offset1:1
	v_add_u32_e32 v1, 0x1458, v48
	ds_write2_b32 v1, v94, v95 offset1:1
	v_add_u32_e32 v1, 0x1860, v48
	v_mov_b32_e32 v90, v3
	v_mov_b32_e32 v91, v3
	s_waitcnt vmcnt(9)
	ds_write2_b32 v1, v96, v97 offset1:1
	v_add_u32_e32 v1, 0x1868, v48
	ds_write2_b32 v1, v98, v99 offset1:1
	v_add_u32_e32 v1, 0x1c70, v48
	s_waitcnt vmcnt(8)
	ds_write2_b32 v1, v100, v101 offset1:1
	v_add_u32_e32 v1, 0x1c78, v48
	ds_write2_b32 v1, v102, v103 offset1:1
	v_add_u32_e32 v1, 0x2080, v48
	s_waitcnt vmcnt(7)
	ds_write2_b32 v1, v104, v105 offset1:1
	v_add_u32_e32 v1, 0x2088, v48
	ds_write2_b32 v1, v106, v107 offset1:1
	v_add_u32_e32 v1, 0x2490, v48
	s_waitcnt vmcnt(6)
	ds_write2_b32 v1, v108, v109 offset1:1
	v_add_u32_e32 v1, 0x2498, v48
	ds_write2_b32 v1, v110, v111 offset1:1
	v_add_u32_e32 v1, 0x28a0, v48
	s_waitcnt vmcnt(5)
	ds_write2_b32 v1, v112, v113 offset1:1
	v_add_u32_e32 v1, 0x28a8, v48
	ds_write2_b32 v1, v114, v115 offset1:1
	v_add_u32_e32 v1, 0x2cb0, v48
	s_waitcnt vmcnt(4)
	ds_write2_b32 v1, v116, v117 offset1:1
	v_add_u32_e32 v1, 0x2cb8, v48
	ds_write2_b32 v1, v118, v119 offset1:1
	v_add_u32_e32 v1, 0x30c0, v48
	s_waitcnt vmcnt(3)
	ds_write2_b32 v1, v120, v121 offset1:1
	v_add_u32_e32 v1, 0x30c8, v48
	ds_write2_b32 v1, v122, v123 offset1:1
	v_add_u32_e32 v1, 0x34d0, v48
	s_waitcnt vmcnt(2)
	ds_write2_b32 v1, v124, v125 offset1:1
	v_add_u32_e32 v1, 0x34d8, v48
	ds_write2_b32 v1, v126, v127 offset1:1
	v_add_u32_e32 v1, 0x38e0, v48
	s_waitcnt vmcnt(1)
	ds_write2_b32 v1, v128, v129 offset1:1
	v_add_u32_e32 v1, 0x38e8, v48
	ds_write2_b32 v1, v130, v131 offset1:1
	v_add_u32_e32 v1, 0x3cf0, v48
	s_waitcnt vmcnt(0)
	ds_write2_b32 v1, v132, v133 offset1:1
	v_add_u32_e32 v1, 0x3cf8, v48
	ds_write2_b32 v1, v134, v135 offset1:1
	s_waitcnt lgkmcnt(0)
	ds_read2_b32 v[42:43], v49 offset0:65 offset1:73
	ds_read2_b32 v[76:77], v49 offset0:130 offset1:138
	ds_read2_b32 v[78:79], v49 offset0:195 offset1:203
	v_add_u32_e32 v1, 0x400, v49
	ds_read2_b32 v[80:81], v49 offset1:8
	ds_read2_b32 v[82:83], v1 offset0:4 offset1:12
	ds_read2_b32 v[84:85], v1 offset0:69 offset1:77
	ds_read2_b32 v[86:87], v1 offset0:134 offset1:142
	ds_read2_b32 v[88:89], v1 offset0:199 offset1:207
	s_waitcnt lgkmcnt(4)
	v_mul_f32_e32 v40, 0x41800000, v80
	v_mul_f32_e32 v41, 0x41800000, v42
	v_med3_f32 v40, v40, s87, v74
	v_med3_f32 v41, v41, s87, v74
	v_cvt_pk_fp8_f32 v90, v40, v41
	v_mul_f32_e32 v42, 0x41800000, v76
	v_mul_f32_e32 v75, 0x41800000, v78
	v_med3_f32 v42, v42, s87, v74
	v_med3_f32 v75, v75, s87, v74
	v_cvt_pk_fp8_f32 v90, v42, v75 op_sel:[0,0,1]
	v_mul_f32_e32 v42, 0x41800000, v81
	s_waitcnt lgkmcnt(3)
	v_mul_f32_e32 v76, 0x41800000, v82
	s_waitcnt lgkmcnt(2)
	v_mul_f32_e32 v78, 0x41800000, v84
	v_med3_f32 v75, v42, s87, v74
	v_mul_f32_e32 v42, 0x41800000, v43
	v_med3_f32 v76, v76, s87, v74
	v_med3_f32 v78, v78, s87, v74
	v_med3_f32 v43, v42, s87, v74
	v_mul_f32_e32 v42, 0x41800000, v77
	v_cvt_pk_fp8_f32 v91, v76, v78
	v_med3_f32 v76, v42, s87, v74
	v_mul_f32_e32 v42, 0x41800000, v79
	v_med3_f32 v77, v42, s87, v74
	v_mul_f32_e32 v42, 0x41800000, v83
	s_waitcnt lgkmcnt(1)
	v_mul_f32_e32 v80, 0x41800000, v86
	s_waitcnt lgkmcnt(0)
	v_mul_f32_e32 v40, 0x41800000, v88
	v_med3_f32 v78, v42, s87, v74
	v_mul_f32_e32 v42, 0x41800000, v85
	v_med3_f32 v80, v80, s87, v74
	v_med3_f32 v40, v40, s87, v74
	v_med3_f32 v79, v42, s87, v74
	v_mul_f32_e32 v42, 0x41800000, v87
	v_cvt_pk_fp8_f32 v91, v80, v40 op_sel:[0,0,1]
	v_med3_f32 v80, v42, s87, v74
	v_mov_b32_e32 v42, v3
	v_cvt_pk_fp8_f32 v42, v75, v43
	v_mov_b32_e32 v43, v3
	v_cvt_pk_fp8_f32 v43, v78, v79
	v_mul_f32_e32 v75, 0x41800000, v89
	v_med3_f32 v75, v75, s87, v74
	v_cvt_pk_fp8_f32 v42, v76, v77 op_sel:[0,0,1]
	v_cvt_pk_fp8_f32 v43, v80, v75 op_sel:[0,0,1]
	v_lshl_add_u64 v[40:41], s[2:3], 0, v[16:17]
	v_add_co_u32_e32 v76, vcc, s68, v40
	global_store_dwordx2 v[40:41], v[90:91], off
	s_nop 0
	v_addc_co_u32_e32 v77, vcc, 0, v41, vcc
	global_store_dwordx2 v[76:77], v[42:43], off
	ds_read2_b32 v[42:43], v49 offset0:81 offset1:89
	ds_read2_b32 v[76:77], v49 offset0:146 offset1:154
	ds_read2_b32 v[78:79], v49 offset0:211 offset1:219
	ds_read2_b32 v[80:81], v49 offset0:16 offset1:24
	ds_read2_b32 v[82:83], v1 offset0:20 offset1:28
	ds_read2_b32 v[84:85], v1 offset0:85 offset1:93
	ds_read2_b32 v[86:87], v1 offset0:150 offset1:158
	ds_read2_b32 v[88:89], v1 offset0:215 offset1:223
	s_waitcnt lgkmcnt(4)
	v_mul_f32_e32 v75, 0x41800000, v80
	s_waitcnt lgkmcnt(3)
	v_mul_f32_e32 v80, 0x41800000, v82
	s_waitcnt lgkmcnt(2)
	v_mul_f32_e32 v82, 0x41800000, v84
	v_med3_f32 v80, v80, s87, v74
	v_med3_f32 v82, v82, s87, v74
	v_mov_b32_e32 v91, v3
	v_mul_f32_e32 v42, 0x41800000, v42
	v_cvt_pk_fp8_f32 v91, v80, v82
	v_med3_f32 v75, v75, s87, v74
	v_med3_f32 v42, v42, s87, v74
	v_mov_b32_e32 v90, v3
	s_waitcnt lgkmcnt(1)
	v_mul_f32_e32 v84, 0x41800000, v86
	v_cvt_pk_fp8_f32 v90, v75, v42
	s_waitcnt lgkmcnt(0)
	v_mul_f32_e32 v42, 0x41800000, v88
	v_med3_f32 v84, v84, s87, v74
	v_med3_f32 v42, v42, s87, v74
	v_cvt_pk_fp8_f32 v91, v84, v42 op_sel:[0,0,1]
	v_mul_f32_e32 v42, 0x41800000, v81
	v_mul_f32_e32 v76, 0x41800000, v76
	v_mul_f32_e32 v78, 0x41800000, v78
	v_med3_f32 v75, v42, s87, v74
	v_mul_f32_e32 v42, 0x41800000, v43
	v_med3_f32 v76, v76, s87, v74
	v_med3_f32 v78, v78, s87, v74
	v_med3_f32 v43, v42, s87, v74
	v_mul_f32_e32 v42, 0x41800000, v77
	v_cvt_pk_fp8_f32 v90, v76, v78 op_sel:[0,0,1]
	v_med3_f32 v76, v42, s87, v74
	v_mul_f32_e32 v42, 0x41800000, v79
	v_med3_f32 v77, v42, s87, v74
	v_mul_f32_e32 v42, 0x41800000, v83
	v_med3_f32 v78, v42, s87, v74
	v_mul_f32_e32 v42, 0x41800000, v85
	v_med3_f32 v79, v42, s87, v74
	v_mul_f32_e32 v42, 0x41800000, v87
	v_med3_f32 v80, v42, s87, v74
	v_mov_b32_e32 v42, v3
	v_cvt_pk_fp8_f32 v42, v75, v43
	v_mov_b32_e32 v43, v3
	v_cvt_pk_fp8_f32 v43, v78, v79
	v_mul_f32_e32 v75, 0x41800000, v89
	v_med3_f32 v75, v75, s87, v74
	v_add_co_u32_e32 v92, vcc, s88, v40
	v_cvt_pk_fp8_f32 v42, v76, v77 op_sel:[0,0,1]
	v_cvt_pk_fp8_f32 v43, v80, v75 op_sel:[0,0,1]
	v_addc_co_u32_e32 v93, vcc, 0, v41, vcc
	v_add_co_u32_e32 v76, vcc, s92, v40
	global_store_dwordx2 v[92:93], v[90:91], off
	s_nop 0
	v_addc_co_u32_e32 v77, vcc, 0, v41, vcc
	global_store_dwordx2 v[76:77], v[42:43], off
	ds_read2_b32 v[42:43], v49 offset0:97 offset1:105
	ds_read2_b32 v[76:77], v49 offset0:162 offset1:170
	ds_read2_b32 v[78:79], v49 offset0:227 offset1:235
	ds_read2_b32 v[80:81], v49 offset0:32 offset1:40
	ds_read2_b32 v[82:83], v1 offset0:36 offset1:44
	ds_read2_b32 v[84:85], v1 offset0:101 offset1:109
	ds_read2_b32 v[86:87], v1 offset0:166 offset1:174
	ds_read2_b32 v[88:89], v1 offset0:231 offset1:239
	s_waitcnt lgkmcnt(4)
	v_mul_f32_e32 v75, 0x41800000, v80
	s_waitcnt lgkmcnt(3)
	v_mul_f32_e32 v80, 0x41800000, v82
	s_waitcnt lgkmcnt(2)
	v_mul_f32_e32 v82, 0x41800000, v84
	v_med3_f32 v80, v80, s87, v74
	v_med3_f32 v82, v82, s87, v74
	v_mov_b32_e32 v91, v3
	v_mul_f32_e32 v42, 0x41800000, v42
	v_cvt_pk_fp8_f32 v91, v80, v82
	v_med3_f32 v75, v75, s87, v74
	v_med3_f32 v42, v42, s87, v74
	v_mov_b32_e32 v90, v3
	s_waitcnt lgkmcnt(1)
	v_mul_f32_e32 v84, 0x41800000, v86
	v_cvt_pk_fp8_f32 v90, v75, v42
	s_waitcnt lgkmcnt(0)
	v_mul_f32_e32 v42, 0x41800000, v88
	v_med3_f32 v84, v84, s87, v74
	v_med3_f32 v42, v42, s87, v74
	v_cvt_pk_fp8_f32 v91, v84, v42 op_sel:[0,0,1]
	v_mul_f32_e32 v42, 0x41800000, v81
	v_mul_f32_e32 v76, 0x41800000, v76
	v_mul_f32_e32 v78, 0x41800000, v78
	v_med3_f32 v75, v42, s87, v74
	v_mul_f32_e32 v42, 0x41800000, v43
	v_med3_f32 v76, v76, s87, v74
	v_med3_f32 v78, v78, s87, v74
	v_med3_f32 v43, v42, s87, v74
	v_mul_f32_e32 v42, 0x41800000, v77
	v_cvt_pk_fp8_f32 v90, v76, v78 op_sel:[0,0,1]
	v_med3_f32 v76, v42, s87, v74
	v_mul_f32_e32 v42, 0x41800000, v79
	v_med3_f32 v77, v42, s87, v74
	v_mul_f32_e32 v42, 0x41800000, v83
	v_med3_f32 v78, v42, s87, v74
	v_mul_f32_e32 v42, 0x41800000, v85
	v_med3_f32 v79, v42, s87, v74
	v_mul_f32_e32 v42, 0x41800000, v87
	v_med3_f32 v80, v42, s87, v74
	v_mov_b32_e32 v42, v3
	v_cvt_pk_fp8_f32 v42, v75, v43
	v_mov_b32_e32 v43, v3
	v_cvt_pk_fp8_f32 v43, v78, v79
	v_mul_f32_e32 v75, 0x41800000, v89
	v_med3_f32 v75, v75, s87, v74
	v_add_co_u32_e32 v92, vcc, s89, v40
	v_cvt_pk_fp8_f32 v42, v76, v77 op_sel:[0,0,1]
	v_cvt_pk_fp8_f32 v43, v80, v75 op_sel:[0,0,1]
	v_addc_co_u32_e32 v93, vcc, 0, v41, vcc
	v_add_co_u32_e32 v76, vcc, s93, v40
	global_store_dwordx2 v[92:93], v[90:91], off
	s_nop 0
	v_addc_co_u32_e32 v77, vcc, 0, v41, vcc
	global_store_dwordx2 v[76:77], v[42:43], off
	ds_read2_b32 v[42:43], v49 offset0:113 offset1:121
	ds_read2_b32 v[76:77], v49 offset0:178 offset1:186
	ds_read2_b32 v[78:79], v49 offset0:243 offset1:251
	ds_read2_b32 v[80:81], v49 offset0:48 offset1:56
	ds_read2_b32 v[82:83], v1 offset0:52 offset1:60
	ds_read2_b32 v[84:85], v1 offset0:117 offset1:125
	ds_read2_b32 v[86:87], v1 offset0:182 offset1:190
	ds_read2_b32 v[88:89], v1 offset0:247 offset1:255
	s_waitcnt lgkmcnt(4)
	v_mul_f32_e32 v1, 0x41800000, v80
	v_mul_f32_e32 v42, 0x41800000, v42
	v_med3_f32 v1, v1, s87, v74
	v_med3_f32 v42, v42, s87, v74
	v_mov_b32_e32 v90, v3
	v_cvt_pk_fp8_f32 v90, v1, v42
	v_mul_f32_e32 v75, 0x41800000, v76
	v_mul_f32_e32 v76, 0x41800000, v78
	s_waitcnt lgkmcnt(3)
	v_mul_f32_e32 v78, 0x41800000, v82
	s_waitcnt lgkmcnt(2)
	v_mul_f32_e32 v80, 0x41800000, v84
	v_med3_f32 v78, v78, s87, v74
	v_med3_f32 v80, v80, s87, v74
	v_mov_b32_e32 v91, v3
	v_mul_f32_e32 v42, 0x41800000, v43
	v_med3_f32 v75, v75, s87, v74
	v_med3_f32 v76, v76, s87, v74
	v_cvt_pk_fp8_f32 v91, v78, v80
	v_med3_f32 v43, v42, s87, v74
	v_mul_f32_e32 v42, 0x41800000, v77
	v_cvt_pk_fp8_f32 v90, v75, v76 op_sel:[0,0,1]
	v_med3_f32 v75, v42, s87, v74
	v_mul_f32_e32 v42, 0x41800000, v79
	s_waitcnt lgkmcnt(1)
	v_mul_f32_e32 v82, 0x41800000, v86
	s_waitcnt lgkmcnt(0)
	v_mul_f32_e32 v1, 0x41800000, v88
	v_med3_f32 v76, v42, s87, v74
	v_mul_f32_e32 v42, 0x41800000, v83
	v_med3_f32 v82, v82, s87, v74
	v_med3_f32 v1, v1, s87, v74
	v_med3_f32 v77, v42, s87, v74
	v_mul_f32_e32 v42, 0x41800000, v85
	v_cvt_pk_fp8_f32 v91, v82, v1 op_sel:[0,0,1]
	v_mul_f32_e32 v1, 0x41800000, v81
	v_med3_f32 v78, v42, s87, v74
	v_mul_f32_e32 v42, 0x41800000, v87
	v_med3_f32 v1, v1, s87, v74
	v_med3_f32 v79, v42, s87, v74
	v_mov_b32_e32 v42, v3
	v_cvt_pk_fp8_f32 v42, v1, v43
	v_mov_b32_e32 v43, v3
	v_cvt_pk_fp8_f32 v43, v77, v78
	v_mul_f32_e32 v1, 0x41800000, v89
	v_med3_f32 v1, v1, s87, v74
	v_add_co_u32_e32 v92, vcc, s90, v40
	v_cvt_pk_fp8_f32 v42, v75, v76 op_sel:[0,0,1]
	v_cvt_pk_fp8_f32 v43, v79, v1 op_sel:[0,0,1]
	v_addc_co_u32_e32 v93, vcc, 0, v41, vcc
	v_add_co_u32_e32 v40, vcc, 0x1c000, v40
	global_store_dwordx2 v[92:93], v[90:91], off
	s_nop 0
	v_addc_co_u32_e32 v41, vcc, 0, v41, vcc
	global_store_dwordx2 v[40:41], v[42:43], off
	s_waitcnt lgkmcnt(0)

.LBB0_263:
	s_andn2_b64 vcc, exec, s[2:3]
	s_cbranch_vccnz .LBB0_265
	s_and_b32 s2, s80, 0x3fc0
	s_add_i32 s34, s2, 0xffffdc00
	s_lshl_b64 s[2:3], s[34:35], 13
	s_add_u32 s2, s58, s2
	s_addc_u32 s3, s59, s3
	s_and_b32 s4, s95, 0x7c0
	s_lshl_b32 s5, s4, 2
	s_add_u32 s2, s2, s5
	s_addc_u32 s3, s3, 0
	v_lshl_add_u64 v[132:133], s[2:3], 0, v[10:11]
	v_add_co_u32_e32 v76, vcc, s88, v132
	s_mov_b32 s2, 0x28000
	s_nop 0
	v_addc_co_u32_e32 v77, vcc, 0, v133, vcc
	v_add_co_u32_e32 v80, vcc, s89, v132
	global_load_dwordx4 v[40:43], v[132:133], off nt
	s_nop 0
	global_load_dwordx4 v[76:79], v[76:77], off nt
	v_addc_co_u32_e32 v81, vcc, 0, v133, vcc
	v_add_co_u32_e32 v84, vcc, s90, v132
	v_add_u32_e32 v1, 0x410, v48
	s_nop 0
	v_addc_co_u32_e32 v85, vcc, 0, v133, vcc
	global_load_dwordx4 v[80:83], v[80:81], off nt
	s_nop 0
	global_load_dwordx4 v[84:87], v[84:85], off nt
	v_add_co_u32_e32 v88, vcc, s91, v132
	v_readlane_b32 s3, v255, 9
	s_nop 0
	v_addc_co_u32_e32 v89, vcc, 0, v133, vcc
	v_add_co_u32_e32 v92, vcc, s2, v132
	s_mov_b32 s2, 0x30000
	s_nop 0
	v_addc_co_u32_e32 v93, vcc, 0, v133, vcc
	global_load_dwordx4 v[88:91], v[88:89], off nt
	s_nop 0
	global_load_dwordx4 v[92:95], v[92:93], off nt
	v_add_co_u32_e32 v96, vcc, s2, v132
	s_lshl_b32 s2, s4, 11
	s_nop 0
	v_addc_co_u32_e32 v97, vcc, 0, v133, vcc
	v_add_co_u32_e32 v100, vcc, s94, v132
	s_add_u32 s2, s3, s2
	s_nop 0
	v_addc_co_u32_e32 v101, vcc, 0, v133, vcc
	global_load_dwordx4 v[96:99], v[96:97], off nt
	s_nop 0
	global_load_dwordx4 v[100:103], v[100:101], off nt
	v_add_co_u32_e32 v104, vcc, s1, v132
	v_readlane_b32 s3, v255, 10
	s_nop 0
	v_addc_co_u32_e32 v105, vcc, 0, v133, vcc
	v_add_co_u32_e32 v108, vcc, s0, v132
	s_addc_u32 s3, s3, 0
	s_nop 0
	v_addc_co_u32_e32 v109, vcc, 0, v133, vcc
	global_load_dwordx4 v[104:107], v[104:105], off nt
	s_nop 0
	global_load_dwordx4 v[108:111], v[108:109], off nt
	v_add_co_u32_e32 v112, vcc, s78, v132
	s_add_u32 s2, s2, s34
	s_nop 0
	v_addc_co_u32_e32 v113, vcc, 0, v133, vcc
	v_add_co_u32_e32 v116, vcc, s79, v132
	s_addc_u32 s3, s3, 0
	s_nop 0
	v_addc_co_u32_e32 v117, vcc, 0, v133, vcc
	global_load_dwordx4 v[112:115], v[112:113], off nt
	s_nop 0
	global_load_dwordx4 v[116:119], v[116:117], off nt
	v_add_co_u32_e32 v120, vcc, s30, v132
	s_nop 1
	v_addc_co_u32_e32 v121, vcc, 0, v133, vcc
	global_load_dwordx4 v[120:123], v[120:121], off nt
	v_add_co_u32_e32 v124, vcc, s31, v132
	s_nop 1
	v_addc_co_u32_e32 v125, vcc, 0, v133, vcc
	global_load_dwordx4 v[124:127], v[124:125], off nt
	v_add_co_u32_e32 v128, vcc, s73, v132
	s_nop 1
	v_addc_co_u32_e32 v129, vcc, 0, v133, vcc
	global_load_dwordx4 v[128:131], v[128:129], off nt
	v_add_co_u32_e32 v132, vcc, s77, v132
	s_nop 1
	v_addc_co_u32_e32 v133, vcc, 0, v133, vcc
	global_load_dwordx4 v[132:135], v[132:133], off nt
	s_waitcnt vmcnt(15)
	ds_write2_b32 v48, v40, v41 offset1:1
	ds_write2_b32 v48, v42, v43 offset0:2 offset1:3
	s_waitcnt vmcnt(14)
	ds_write2_b32 v1, v76, v77 offset1:1
	v_add_u32_e32 v1, 0x418, v48
	ds_write2_b32 v1, v78, v79 offset1:1
	v_add_u32_e32 v1, 0x820, v48
	s_waitcnt vmcnt(13)
	ds_write2_b32 v1, v80, v81 offset1:1
	v_add_u32_e32 v1, 0x828, v48
	ds_write2_b32 v1, v82, v83 offset1:1
	v_add_u32_e32 v1, 0xc30, v48
	s_waitcnt vmcnt(12)
	ds_write2_b32 v1, v84, v85 offset1:1
	v_add_u32_e32 v1, 0xc38, v48
	ds_write2_b32 v1, v86, v87 offset1:1
	v_add_u32_e32 v1, 0x1040, v48
	s_waitcnt vmcnt(11)
	ds_write2_b32 v1, v88, v89 offset1:1
	v_add_u32_e32 v1, 0x1048, v48
	ds_write2_b32 v1, v90, v91 offset1:1
	v_add_u32_e32 v1, 0x1450, v48
	s_waitcnt vmcnt(10)
	ds_write2_b32 v1, v92, v93 offset1:1
	v_add_u32_e32 v1, 0x1458, v48
	ds_write2_b32 v1, v94, v95 offset1:1
	v_add_u32_e32 v1, 0x1860, v48
	v_mov_b32_e32 v90, v3
	v_mov_b32_e32 v91, v3
	s_waitcnt vmcnt(9)
	ds_write2_b32 v1, v96, v97 offset1:1
	v_add_u32_e32 v1, 0x1868, v48
	ds_write2_b32 v1, v98, v99 offset1:1
	v_add_u32_e32 v1, 0x1c70, v48
	s_waitcnt vmcnt(8)
	ds_write2_b32 v1, v100, v101 offset1:1
	v_add_u32_e32 v1, 0x1c78, v48
	ds_write2_b32 v1, v102, v103 offset1:1
	v_add_u32_e32 v1, 0x2080, v48
	s_waitcnt vmcnt(7)
	ds_write2_b32 v1, v104, v105 offset1:1
	v_add_u32_e32 v1, 0x2088, v48
	ds_write2_b32 v1, v106, v107 offset1:1
	v_add_u32_e32 v1, 0x2490, v48
	s_waitcnt vmcnt(6)
	ds_write2_b32 v1, v108, v109 offset1:1
	v_add_u32_e32 v1, 0x2498, v48
	ds_write2_b32 v1, v110, v111 offset1:1
	v_add_u32_e32 v1, 0x28a0, v48
	s_waitcnt vmcnt(5)
	ds_write2_b32 v1, v112, v113 offset1:1
	v_add_u32_e32 v1, 0x28a8, v48
	ds_write2_b32 v1, v114, v115 offset1:1
	v_add_u32_e32 v1, 0x2cb0, v48
	s_waitcnt vmcnt(4)
	ds_write2_b32 v1, v116, v117 offset1:1
	v_add_u32_e32 v1, 0x2cb8, v48
	ds_write2_b32 v1, v118, v119 offset1:1
	v_add_u32_e32 v1, 0x30c0, v48
	s_waitcnt vmcnt(3)
	ds_write2_b32 v1, v120, v121 offset1:1
	v_add_u32_e32 v1, 0x30c8, v48
	ds_write2_b32 v1, v122, v123 offset1:1
	v_add_u32_e32 v1, 0x34d0, v48
	s_waitcnt vmcnt(2)
	ds_write2_b32 v1, v124, v125 offset1:1
	v_add_u32_e32 v1, 0x34d8, v48
	ds_write2_b32 v1, v126, v127 offset1:1
	v_add_u32_e32 v1, 0x38e0, v48
	s_waitcnt vmcnt(1)
	ds_write2_b32 v1, v128, v129 offset1:1
	v_add_u32_e32 v1, 0x38e8, v48
	ds_write2_b32 v1, v130, v131 offset1:1
	v_add_u32_e32 v1, 0x3cf0, v48
	s_waitcnt vmcnt(0)
	ds_write2_b32 v1, v132, v133 offset1:1
	v_add_u32_e32 v1, 0x3cf8, v48
	ds_write2_b32 v1, v134, v135 offset1:1
	s_waitcnt lgkmcnt(0)
	ds_read2_b32 v[42:43], v49 offset0:65 offset1:73
	ds_read2_b32 v[76:77], v49 offset0:130 offset1:138
	ds_read2_b32 v[78:79], v49 offset0:195 offset1:203
	v_add_u32_e32 v1, 0x400, v49
	ds_read2_b32 v[80:81], v49 offset1:8
	ds_read2_b32 v[82:83], v1 offset0:4 offset1:12
	ds_read2_b32 v[84:85], v1 offset0:69 offset1:77
	ds_read2_b32 v[86:87], v1 offset0:134 offset1:142
	ds_read2_b32 v[88:89], v1 offset0:199 offset1:207
	s_waitcnt lgkmcnt(4)
	v_mul_f32_e32 v40, 0x41800000, v80
	v_mul_f32_e32 v41, 0x41800000, v42
	v_med3_f32 v40, v40, s87, v74
	v_med3_f32 v41, v41, s87, v74
	v_cvt_pk_fp8_f32 v90, v40, v41
	v_mul_f32_e32 v42, 0x41800000, v76
	v_mul_f32_e32 v75, 0x41800000, v78
	v_med3_f32 v42, v42, s87, v74
	v_med3_f32 v75, v75, s87, v74
	v_cvt_pk_fp8_f32 v90, v42, v75 op_sel:[0,0,1]
	v_mul_f32_e32 v42, 0x41800000, v81
	s_waitcnt lgkmcnt(3)
	v_mul_f32_e32 v76, 0x41800000, v82
	s_waitcnt lgkmcnt(2)
	v_mul_f32_e32 v78, 0x41800000, v84
	v_med3_f32 v75, v42, s87, v74
	v_mul_f32_e32 v42, 0x41800000, v43
	v_med3_f32 v76, v76, s87, v74
	v_med3_f32 v78, v78, s87, v74
	v_med3_f32 v43, v42, s87, v74
	v_mul_f32_e32 v42, 0x41800000, v77
	v_cvt_pk_fp8_f32 v91, v76, v78
	v_med3_f32 v76, v42, s87, v74
	v_mul_f32_e32 v42, 0x41800000, v79
	v_med3_f32 v77, v42, s87, v74
	v_mul_f32_e32 v42, 0x41800000, v83
	s_waitcnt lgkmcnt(1)
	v_mul_f32_e32 v80, 0x41800000, v86
	s_waitcnt lgkmcnt(0)
	v_mul_f32_e32 v40, 0x41800000, v88
	v_med3_f32 v78, v42, s87, v74
	v_mul_f32_e32 v42, 0x41800000, v85
	v_med3_f32 v80, v80, s87, v74
	v_med3_f32 v40, v40, s87, v74
	v_med3_f32 v79, v42, s87, v74
	v_mul_f32_e32 v42, 0x41800000, v87
	v_cvt_pk_fp8_f32 v91, v80, v40 op_sel:[0,0,1]
	v_med3_f32 v80, v42, s87, v74
	v_mov_b32_e32 v42, v3
	v_cvt_pk_fp8_f32 v42, v75, v43
	v_mov_b32_e32 v43, v3
	v_cvt_pk_fp8_f32 v43, v78, v79
	v_mul_f32_e32 v75, 0x41800000, v89
	v_med3_f32 v75, v75, s87, v74
	v_cvt_pk_fp8_f32 v42, v76, v77 op_sel:[0,0,1]
	v_cvt_pk_fp8_f32 v43, v80, v75 op_sel:[0,0,1]
	v_lshl_add_u64 v[40:41], s[2:3], 0, v[16:17]
	v_add_co_u32_e32 v76, vcc, s68, v40
	global_store_dwordx2 v[40:41], v[90:91], off
	s_nop 0
	v_addc_co_u32_e32 v77, vcc, 0, v41, vcc
	global_store_dwordx2 v[76:77], v[42:43], off
	ds_read2_b32 v[42:43], v49 offset0:81 offset1:89
	ds_read2_b32 v[76:77], v49 offset0:146 offset1:154
	ds_read2_b32 v[78:79], v49 offset0:211 offset1:219
	ds_read2_b32 v[80:81], v49 offset0:16 offset1:24
	ds_read2_b32 v[82:83], v1 offset0:20 offset1:28
	ds_read2_b32 v[84:85], v1 offset0:85 offset1:93
	ds_read2_b32 v[86:87], v1 offset0:150 offset1:158
	ds_read2_b32 v[88:89], v1 offset0:215 offset1:223
	s_waitcnt lgkmcnt(4)
	v_mul_f32_e32 v75, 0x41800000, v80
	s_waitcnt lgkmcnt(3)
	v_mul_f32_e32 v80, 0x41800000, v82
	s_waitcnt lgkmcnt(2)
	v_mul_f32_e32 v82, 0x41800000, v84
	v_med3_f32 v80, v80, s87, v74
	v_med3_f32 v82, v82, s87, v74
	v_mov_b32_e32 v91, v3
	v_mul_f32_e32 v42, 0x41800000, v42
	v_cvt_pk_fp8_f32 v91, v80, v82
	v_med3_f32 v75, v75, s87, v74
	v_med3_f32 v42, v42, s87, v74
	v_mov_b32_e32 v90, v3
	s_waitcnt lgkmcnt(1)
	v_mul_f32_e32 v84, 0x41800000, v86
	v_cvt_pk_fp8_f32 v90, v75, v42
	s_waitcnt lgkmcnt(0)
	v_mul_f32_e32 v42, 0x41800000, v88
	v_med3_f32 v84, v84, s87, v74
	v_med3_f32 v42, v42, s87, v74
	v_cvt_pk_fp8_f32 v91, v84, v42 op_sel:[0,0,1]
	v_mul_f32_e32 v42, 0x41800000, v81
	v_mul_f32_e32 v76, 0x41800000, v76
	v_mul_f32_e32 v78, 0x41800000, v78
	v_med3_f32 v75, v42, s87, v74
	v_mul_f32_e32 v42, 0x41800000, v43
	v_med3_f32 v76, v76, s87, v74
	v_med3_f32 v78, v78, s87, v74
	v_med3_f32 v43, v42, s87, v74
	v_mul_f32_e32 v42, 0x41800000, v77
	v_cvt_pk_fp8_f32 v90, v76, v78 op_sel:[0,0,1]
	v_med3_f32 v76, v42, s87, v74
	v_mul_f32_e32 v42, 0x41800000, v79
	v_med3_f32 v77, v42, s87, v74
	v_mul_f32_e32 v42, 0x41800000, v83
	v_med3_f32 v78, v42, s87, v74
	v_mul_f32_e32 v42, 0x41800000, v85
	v_med3_f32 v79, v42, s87, v74
	v_mul_f32_e32 v42, 0x41800000, v87
	v_med3_f32 v80, v42, s87, v74
	v_mov_b32_e32 v42, v3
	v_cvt_pk_fp8_f32 v42, v75, v43
	v_mov_b32_e32 v43, v3
	v_cvt_pk_fp8_f32 v43, v78, v79
	v_mul_f32_e32 v75, 0x41800000, v89
	v_med3_f32 v75, v75, s87, v74
	v_add_co_u32_e32 v92, vcc, s88, v40
	v_cvt_pk_fp8_f32 v42, v76, v77 op_sel:[0,0,1]
	v_cvt_pk_fp8_f32 v43, v80, v75 op_sel:[0,0,1]
	v_addc_co_u32_e32 v93, vcc, 0, v41, vcc
	v_add_co_u32_e32 v76, vcc, s92, v40
	global_store_dwordx2 v[92:93], v[90:91], off
	s_nop 0
	v_addc_co_u32_e32 v77, vcc, 0, v41, vcc
	global_store_dwordx2 v[76:77], v[42:43], off
	ds_read2_b32 v[42:43], v49 offset0:97 offset1:105
	ds_read2_b32 v[76:77], v49 offset0:162 offset1:170
	ds_read2_b32 v[78:79], v49 offset0:227 offset1:235
	ds_read2_b32 v[80:81], v49 offset0:32 offset1:40
	ds_read2_b32 v[82:83], v1 offset0:36 offset1:44
	ds_read2_b32 v[84:85], v1 offset0:101 offset1:109
	ds_read2_b32 v[86:87], v1 offset0:166 offset1:174
	ds_read2_b32 v[88:89], v1 offset0:231 offset1:239
	s_waitcnt lgkmcnt(4)
	v_mul_f32_e32 v75, 0x41800000, v80
	s_waitcnt lgkmcnt(3)
	v_mul_f32_e32 v80, 0x41800000, v82
	s_waitcnt lgkmcnt(2)
	v_mul_f32_e32 v82, 0x41800000, v84
	v_med3_f32 v80, v80, s87, v74
	v_med3_f32 v82, v82, s87, v74
	v_mov_b32_e32 v91, v3
	v_mul_f32_e32 v42, 0x41800000, v42
	v_cvt_pk_fp8_f32 v91, v80, v82
	v_med3_f32 v75, v75, s87, v74
	v_med3_f32 v42, v42, s87, v74
	v_mov_b32_e32 v90, v3
	s_waitcnt lgkmcnt(1)
	v_mul_f32_e32 v84, 0x41800000, v86
	v_cvt_pk_fp8_f32 v90, v75, v42
	s_waitcnt lgkmcnt(0)
	v_mul_f32_e32 v42, 0x41800000, v88
	v_med3_f32 v84, v84, s87, v74
	v_med3_f32 v42, v42, s87, v74
	v_cvt_pk_fp8_f32 v91, v84, v42 op_sel:[0,0,1]
	v_mul_f32_e32 v42, 0x41800000, v81
	v_mul_f32_e32 v76, 0x41800000, v76
	v_mul_f32_e32 v78, 0x41800000, v78
	v_med3_f32 v75, v42, s87, v74
	v_mul_f32_e32 v42, 0x41800000, v43
	v_med3_f32 v76, v76, s87, v74
	v_med3_f32 v78, v78, s87, v74
	v_med3_f32 v43, v42, s87, v74
	v_mul_f32_e32 v42, 0x41800000, v77
	v_cvt_pk_fp8_f32 v90, v76, v78 op_sel:[0,0,1]
	v_med3_f32 v76, v42, s87, v74
	v_mul_f32_e32 v42, 0x41800000, v79
	v_med3_f32 v77, v42, s87, v74
	v_mul_f32_e32 v42, 0x41800000, v83
	v_med3_f32 v78, v42, s87, v74
	v_mul_f32_e32 v42, 0x41800000, v85
	v_med3_f32 v79, v42, s87, v74
	v_mul_f32_e32 v42, 0x41800000, v87
	v_med3_f32 v80, v42, s87, v74
	v_mov_b32_e32 v42, v3
	v_cvt_pk_fp8_f32 v42, v75, v43
	v_mov_b32_e32 v43, v3
	v_cvt_pk_fp8_f32 v43, v78, v79
	v_mul_f32_e32 v75, 0x41800000, v89
	v_med3_f32 v75, v75, s87, v74
	v_add_co_u32_e32 v92, vcc, s89, v40
	v_cvt_pk_fp8_f32 v42, v76, v77 op_sel:[0,0,1]
	v_cvt_pk_fp8_f32 v43, v80, v75 op_sel:[0,0,1]
	v_addc_co_u32_e32 v93, vcc, 0, v41, vcc
	v_add_co_u32_e32 v76, vcc, s93, v40
	global_store_dwordx2 v[92:93], v[90:91], off
	s_nop 0
	v_addc_co_u32_e32 v77, vcc, 0, v41, vcc
	global_store_dwordx2 v[76:77], v[42:43], off
	ds_read2_b32 v[42:43], v49 offset0:113 offset1:121
	ds_read2_b32 v[76:77], v49 offset0:178 offset1:186
	ds_read2_b32 v[78:79], v49 offset0:243 offset1:251
	ds_read2_b32 v[80:81], v49 offset0:48 offset1:56
	ds_read2_b32 v[82:83], v1 offset0:52 offset1:60
	ds_read2_b32 v[84:85], v1 offset0:117 offset1:125
	ds_read2_b32 v[86:87], v1 offset0:182 offset1:190
	ds_read2_b32 v[88:89], v1 offset0:247 offset1:255
	s_waitcnt lgkmcnt(4)
	v_mul_f32_e32 v1, 0x41800000, v80
	v_mul_f32_e32 v42, 0x41800000, v42
	v_med3_f32 v1, v1, s87, v74
	v_med3_f32 v42, v42, s87, v74
	v_mov_b32_e32 v90, v3
	v_cvt_pk_fp8_f32 v90, v1, v42
	v_mul_f32_e32 v75, 0x41800000, v76
	v_mul_f32_e32 v76, 0x41800000, v78
	s_waitcnt lgkmcnt(3)
	v_mul_f32_e32 v78, 0x41800000, v82
	s_waitcnt lgkmcnt(2)
	v_mul_f32_e32 v80, 0x41800000, v84
	v_med3_f32 v78, v78, s87, v74
	v_med3_f32 v80, v80, s87, v74
	v_mov_b32_e32 v91, v3
	v_mul_f32_e32 v42, 0x41800000, v43
	v_med3_f32 v75, v75, s87, v74
	v_med3_f32 v76, v76, s87, v74
	v_cvt_pk_fp8_f32 v91, v78, v80
	v_med3_f32 v43, v42, s87, v74
	v_mul_f32_e32 v42, 0x41800000, v77
	v_cvt_pk_fp8_f32 v90, v75, v76 op_sel:[0,0,1]
	v_med3_f32 v75, v42, s87, v74
	v_mul_f32_e32 v42, 0x41800000, v79
	s_waitcnt lgkmcnt(1)
	v_mul_f32_e32 v82, 0x41800000, v86
	s_waitcnt lgkmcnt(0)
	v_mul_f32_e32 v1, 0x41800000, v88
	v_med3_f32 v76, v42, s87, v74
	v_mul_f32_e32 v42, 0x41800000, v83
	v_med3_f32 v82, v82, s87, v74
	v_med3_f32 v1, v1, s87, v74
	v_med3_f32 v77, v42, s87, v74
	v_mul_f32_e32 v42, 0x41800000, v85
	v_cvt_pk_fp8_f32 v91, v82, v1 op_sel:[0,0,1]
	v_mul_f32_e32 v1, 0x41800000, v81
	v_med3_f32 v78, v42, s87, v74
	v_mul_f32_e32 v42, 0x41800000, v87
	v_med3_f32 v1, v1, s87, v74
	v_med3_f32 v79, v42, s87, v74
	v_mov_b32_e32 v42, v3
	v_cvt_pk_fp8_f32 v42, v1, v43
	v_mov_b32_e32 v43, v3
	v_cvt_pk_fp8_f32 v43, v77, v78
	v_mul_f32_e32 v1, 0x41800000, v89
	v_med3_f32 v1, v1, s87, v74
	v_add_co_u32_e32 v92, vcc, s90, v40
	v_cvt_pk_fp8_f32 v42, v75, v76 op_sel:[0,0,1]
	v_cvt_pk_fp8_f32 v43, v79, v1 op_sel:[0,0,1]
	v_addc_co_u32_e32 v93, vcc, 0, v41, vcc
	v_add_co_u32_e32 v40, vcc, 0x1c000, v40
	global_store_dwordx2 v[92:93], v[90:91], off
	s_nop 0
	v_addc_co_u32_e32 v41, vcc, 0, v41, vcc
	global_store_dwordx2 v[40:41], v[42:43], off
	s_waitcnt lgkmcnt(0)

.LBB0_266:
	s_andn2_b64 vcc, exec, s[2:3]
	s_cbranch_vccnz .LBB0_268
	s_and_b32 s2, s80, 0x3fc0
	s_add_i32 s34, s2, 0xffffe000
	s_lshl_b64 s[2:3], s[34:35], 13
	s_add_u32 s2, s56, s2
	s_addc_u32 s3, s57, s3
	s_and_b32 s4, s95, 0x7c0
	s_lshl_b32 s5, s4, 2
	s_add_u32 s2, s2, s5
	s_addc_u32 s3, s3, 0
	v_lshl_add_u64 v[132:133], s[2:3], 0, v[10:11]
	v_add_co_u32_e32 v76, vcc, s88, v132
	s_mov_b32 s2, 0x28000
	s_nop 0
	v_addc_co_u32_e32 v77, vcc, 0, v133, vcc
	v_add_co_u32_e32 v80, vcc, s89, v132
	global_load_dwordx4 v[40:43], v[132:133], off nt
	s_nop 0
	global_load_dwordx4 v[76:79], v[76:77], off nt
	v_addc_co_u32_e32 v81, vcc, 0, v133, vcc
	v_add_co_u32_e32 v84, vcc, s90, v132
	v_add_u32_e32 v1, 0x410, v48
	s_nop 0
	v_addc_co_u32_e32 v85, vcc, 0, v133, vcc
	global_load_dwordx4 v[80:83], v[80:81], off nt
	s_nop 0
	global_load_dwordx4 v[84:87], v[84:85], off nt
	v_add_co_u32_e32 v88, vcc, s91, v132
	s_nop 1
	v_addc_co_u32_e32 v89, vcc, 0, v133, vcc
	v_add_co_u32_e32 v92, vcc, s2, v132
	s_mov_b32 s2, 0x30000
	s_nop 0
	v_addc_co_u32_e32 v93, vcc, 0, v133, vcc
	global_load_dwordx4 v[88:91], v[88:89], off nt
	s_nop 0
	global_load_dwordx4 v[92:95], v[92:93], off nt
	v_add_co_u32_e32 v96, vcc, s2, v132
	s_lshl_b32 s2, s4, 11
	s_nop 0
	v_addc_co_u32_e32 v97, vcc, 0, v133, vcc
	v_add_co_u32_e32 v100, vcc, s94, v132
	s_add_u32 s2, s69, s2
	s_nop 0
	v_addc_co_u32_e32 v101, vcc, 0, v133, vcc
	global_load_dwordx4 v[96:99], v[96:97], off nt
	s_nop 0
	global_load_dwordx4 v[100:103], v[100:101], off nt
	v_add_co_u32_e32 v104, vcc, s1, v132
	s_addc_u32 s3, s72, 0
	s_nop 0
	v_addc_co_u32_e32 v105, vcc, 0, v133, vcc
	v_add_co_u32_e32 v108, vcc, s0, v132
	s_add_u32 s2, s2, s34
	s_nop 0
	v_addc_co_u32_e32 v109, vcc, 0, v133, vcc
	global_load_dwordx4 v[104:107], v[104:105], off nt
	s_nop 0
	global_load_dwordx4 v[108:111], v[108:109], off nt
	v_add_co_u32_e32 v112, vcc, s78, v132
	s_addc_u32 s3, s3, 0
	s_nop 0
	v_addc_co_u32_e32 v113, vcc, 0, v133, vcc
	v_add_co_u32_e32 v116, vcc, s79, v132
	s_nop 1
	v_addc_co_u32_e32 v117, vcc, 0, v133, vcc
	global_load_dwordx4 v[112:115], v[112:113], off nt
	s_nop 0
	global_load_dwordx4 v[116:119], v[116:117], off nt
	v_add_co_u32_e32 v120, vcc, s30, v132
	s_nop 1
	v_addc_co_u32_e32 v121, vcc, 0, v133, vcc
	global_load_dwordx4 v[120:123], v[120:121], off nt
	v_add_co_u32_e32 v124, vcc, s31, v132
	s_nop 1
	v_addc_co_u32_e32 v125, vcc, 0, v133, vcc
	global_load_dwordx4 v[124:127], v[124:125], off nt
	v_add_co_u32_e32 v128, vcc, s73, v132
	s_nop 1
	v_addc_co_u32_e32 v129, vcc, 0, v133, vcc
	global_load_dwordx4 v[128:131], v[128:129], off nt
	v_add_co_u32_e32 v132, vcc, s77, v132
	s_nop 1
	v_addc_co_u32_e32 v133, vcc, 0, v133, vcc
	global_load_dwordx4 v[132:135], v[132:133], off nt
	s_waitcnt vmcnt(15)
	ds_write2_b32 v48, v40, v41 offset1:1
	ds_write2_b32 v48, v42, v43 offset0:2 offset1:3
	s_waitcnt vmcnt(14)
	ds_write2_b32 v1, v76, v77 offset1:1
	v_add_u32_e32 v1, 0x418, v48
	ds_write2_b32 v1, v78, v79 offset1:1
	v_add_u32_e32 v1, 0x820, v48
	s_waitcnt vmcnt(13)
	ds_write2_b32 v1, v80, v81 offset1:1
	v_add_u32_e32 v1, 0x828, v48
	ds_write2_b32 v1, v82, v83 offset1:1
	v_add_u32_e32 v1, 0xc30, v48
	s_waitcnt vmcnt(12)
	ds_write2_b32 v1, v84, v85 offset1:1
	v_add_u32_e32 v1, 0xc38, v48
	ds_write2_b32 v1, v86, v87 offset1:1
	v_add_u32_e32 v1, 0x1040, v48
	s_waitcnt vmcnt(11)
	ds_write2_b32 v1, v88, v89 offset1:1
	v_add_u32_e32 v1, 0x1048, v48
	ds_write2_b32 v1, v90, v91 offset1:1
	v_add_u32_e32 v1, 0x1450, v48
	s_waitcnt vmcnt(10)
	ds_write2_b32 v1, v92, v93 offset1:1
	v_add_u32_e32 v1, 0x1458, v48
	ds_write2_b32 v1, v94, v95 offset1:1
	v_add_u32_e32 v1, 0x1860, v48
	v_mov_b32_e32 v90, v3
	v_mov_b32_e32 v91, v3
	s_waitcnt vmcnt(9)
	ds_write2_b32 v1, v96, v97 offset1:1
	v_add_u32_e32 v1, 0x1868, v48
	ds_write2_b32 v1, v98, v99 offset1:1
	v_add_u32_e32 v1, 0x1c70, v48
	s_waitcnt vmcnt(8)
	ds_write2_b32 v1, v100, v101 offset1:1
	v_add_u32_e32 v1, 0x1c78, v48
	ds_write2_b32 v1, v102, v103 offset1:1
	v_add_u32_e32 v1, 0x2080, v48
	s_waitcnt vmcnt(7)
	ds_write2_b32 v1, v104, v105 offset1:1
	v_add_u32_e32 v1, 0x2088, v48
	ds_write2_b32 v1, v106, v107 offset1:1
	v_add_u32_e32 v1, 0x2490, v48
	s_waitcnt vmcnt(6)
	ds_write2_b32 v1, v108, v109 offset1:1
	v_add_u32_e32 v1, 0x2498, v48
	ds_write2_b32 v1, v110, v111 offset1:1
	v_add_u32_e32 v1, 0x28a0, v48
	s_waitcnt vmcnt(5)
	ds_write2_b32 v1, v112, v113 offset1:1
	v_add_u32_e32 v1, 0x28a8, v48
	ds_write2_b32 v1, v114, v115 offset1:1
	v_add_u32_e32 v1, 0x2cb0, v48
	s_waitcnt vmcnt(4)
	ds_write2_b32 v1, v116, v117 offset1:1
	v_add_u32_e32 v1, 0x2cb8, v48
	ds_write2_b32 v1, v118, v119 offset1:1
	v_add_u32_e32 v1, 0x30c0, v48
	s_waitcnt vmcnt(3)
	ds_write2_b32 v1, v120, v121 offset1:1
	v_add_u32_e32 v1, 0x30c8, v48
	ds_write2_b32 v1, v122, v123 offset1:1
	v_add_u32_e32 v1, 0x34d0, v48
	s_waitcnt vmcnt(2)
	ds_write2_b32 v1, v124, v125 offset1:1
	v_add_u32_e32 v1, 0x34d8, v48
	ds_write2_b32 v1, v126, v127 offset1:1
	v_add_u32_e32 v1, 0x38e0, v48
	s_waitcnt vmcnt(1)
	ds_write2_b32 v1, v128, v129 offset1:1
	v_add_u32_e32 v1, 0x38e8, v48
	ds_write2_b32 v1, v130, v131 offset1:1
	v_add_u32_e32 v1, 0x3cf0, v48
	s_waitcnt vmcnt(0)
	ds_write2_b32 v1, v132, v133 offset1:1
	v_add_u32_e32 v1, 0x3cf8, v48
	ds_write2_b32 v1, v134, v135 offset1:1
	s_waitcnt lgkmcnt(0)
	ds_read2_b32 v[42:43], v49 offset0:65 offset1:73
	ds_read2_b32 v[76:77], v49 offset0:130 offset1:138
	ds_read2_b32 v[78:79], v49 offset0:195 offset1:203
	v_add_u32_e32 v1, 0x400, v49
	ds_read2_b32 v[80:81], v49 offset1:8
	ds_read2_b32 v[82:83], v1 offset0:4 offset1:12
	ds_read2_b32 v[84:85], v1 offset0:69 offset1:77
	ds_read2_b32 v[86:87], v1 offset0:134 offset1:142
	ds_read2_b32 v[88:89], v1 offset0:199 offset1:207
	s_waitcnt lgkmcnt(4)
	v_mul_f32_e32 v40, 0x41800000, v80
	v_mul_f32_e32 v41, 0x41800000, v42
	v_med3_f32 v40, v40, s87, v74
	v_med3_f32 v41, v41, s87, v74
	v_cvt_pk_fp8_f32 v90, v40, v41
	v_mul_f32_e32 v42, 0x41800000, v76
	v_mul_f32_e32 v75, 0x41800000, v78
	v_med3_f32 v42, v42, s87, v74
	v_med3_f32 v75, v75, s87, v74
	v_cvt_pk_fp8_f32 v90, v42, v75 op_sel:[0,0,1]
	v_mul_f32_e32 v42, 0x41800000, v81
	s_waitcnt lgkmcnt(3)
	v_mul_f32_e32 v76, 0x41800000, v82
	s_waitcnt lgkmcnt(2)
	v_mul_f32_e32 v78, 0x41800000, v84
	v_med3_f32 v75, v42, s87, v74
	v_mul_f32_e32 v42, 0x41800000, v43
	v_med3_f32 v76, v76, s87, v74
	v_med3_f32 v78, v78, s87, v74
	v_med3_f32 v43, v42, s87, v74
	v_mul_f32_e32 v42, 0x41800000, v77
	v_cvt_pk_fp8_f32 v91, v76, v78
	v_med3_f32 v76, v42, s87, v74
	v_mul_f32_e32 v42, 0x41800000, v79
	v_med3_f32 v77, v42, s87, v74
	v_mul_f32_e32 v42, 0x41800000, v83
	s_waitcnt lgkmcnt(1)
	v_mul_f32_e32 v80, 0x41800000, v86
	s_waitcnt lgkmcnt(0)
	v_mul_f32_e32 v40, 0x41800000, v88
	v_med3_f32 v78, v42, s87, v74
	v_mul_f32_e32 v42, 0x41800000, v85
	v_med3_f32 v80, v80, s87, v74
	v_med3_f32 v40, v40, s87, v74
	v_med3_f32 v79, v42, s87, v74
	v_mul_f32_e32 v42, 0x41800000, v87
	v_cvt_pk_fp8_f32 v91, v80, v40 op_sel:[0,0,1]
	v_med3_f32 v80, v42, s87, v74
	v_mov_b32_e32 v42, v3
	v_cvt_pk_fp8_f32 v42, v75, v43
	v_mov_b32_e32 v43, v3
	v_cvt_pk_fp8_f32 v43, v78, v79
	v_mul_f32_e32 v75, 0x41800000, v89
	v_med3_f32 v75, v75, s87, v74
	v_cvt_pk_fp8_f32 v42, v76, v77 op_sel:[0,0,1]
	v_cvt_pk_fp8_f32 v43, v80, v75 op_sel:[0,0,1]
	v_lshl_add_u64 v[40:41], s[2:3], 0, v[16:17]
	v_add_co_u32_e32 v76, vcc, s68, v40
	global_store_dwordx2 v[40:41], v[90:91], off
	s_nop 0
	v_addc_co_u32_e32 v77, vcc, 0, v41, vcc
	global_store_dwordx2 v[76:77], v[42:43], off
	ds_read2_b32 v[42:43], v49 offset0:81 offset1:89
	ds_read2_b32 v[76:77], v49 offset0:146 offset1:154
	ds_read2_b32 v[78:79], v49 offset0:211 offset1:219
	ds_read2_b32 v[80:81], v49 offset0:16 offset1:24
	ds_read2_b32 v[82:83], v1 offset0:20 offset1:28
	ds_read2_b32 v[84:85], v1 offset0:85 offset1:93
	ds_read2_b32 v[86:87], v1 offset0:150 offset1:158
	ds_read2_b32 v[88:89], v1 offset0:215 offset1:223
	s_waitcnt lgkmcnt(4)
	v_mul_f32_e32 v75, 0x41800000, v80
	s_waitcnt lgkmcnt(3)
	v_mul_f32_e32 v80, 0x41800000, v82
	s_waitcnt lgkmcnt(2)
	v_mul_f32_e32 v82, 0x41800000, v84
	v_med3_f32 v80, v80, s87, v74
	v_med3_f32 v82, v82, s87, v74
	v_mov_b32_e32 v91, v3
	v_mul_f32_e32 v42, 0x41800000, v42
	v_cvt_pk_fp8_f32 v91, v80, v82
	v_med3_f32 v75, v75, s87, v74
	v_med3_f32 v42, v42, s87, v74
	v_mov_b32_e32 v90, v3
	s_waitcnt lgkmcnt(1)
	v_mul_f32_e32 v84, 0x41800000, v86
	v_cvt_pk_fp8_f32 v90, v75, v42
	s_waitcnt lgkmcnt(0)
	v_mul_f32_e32 v42, 0x41800000, v88
	v_med3_f32 v84, v84, s87, v74
	v_med3_f32 v42, v42, s87, v74
	v_cvt_pk_fp8_f32 v91, v84, v42 op_sel:[0,0,1]
	v_mul_f32_e32 v42, 0x41800000, v81
	v_mul_f32_e32 v76, 0x41800000, v76
	v_mul_f32_e32 v78, 0x41800000, v78
	v_med3_f32 v75, v42, s87, v74
	v_mul_f32_e32 v42, 0x41800000, v43
	v_med3_f32 v76, v76, s87, v74
	v_med3_f32 v78, v78, s87, v74
	v_med3_f32 v43, v42, s87, v74
	v_mul_f32_e32 v42, 0x41800000, v77
	v_cvt_pk_fp8_f32 v90, v76, v78 op_sel:[0,0,1]
	v_med3_f32 v76, v42, s87, v74
	v_mul_f32_e32 v42, 0x41800000, v79
	v_med3_f32 v77, v42, s87, v74
	v_mul_f32_e32 v42, 0x41800000, v83
	v_med3_f32 v78, v42, s87, v74
	v_mul_f32_e32 v42, 0x41800000, v85
	v_med3_f32 v79, v42, s87, v74
	v_mul_f32_e32 v42, 0x41800000, v87
	v_med3_f32 v80, v42, s87, v74
	v_mov_b32_e32 v42, v3
	v_cvt_pk_fp8_f32 v42, v75, v43
	v_mov_b32_e32 v43, v3
	v_cvt_pk_fp8_f32 v43, v78, v79
	v_mul_f32_e32 v75, 0x41800000, v89
	v_med3_f32 v75, v75, s87, v74
	v_add_co_u32_e32 v92, vcc, s88, v40
	v_cvt_pk_fp8_f32 v42, v76, v77 op_sel:[0,0,1]
	v_cvt_pk_fp8_f32 v43, v80, v75 op_sel:[0,0,1]
	v_addc_co_u32_e32 v93, vcc, 0, v41, vcc
	v_add_co_u32_e32 v76, vcc, s92, v40
	global_store_dwordx2 v[92:93], v[90:91], off
	s_nop 0
	v_addc_co_u32_e32 v77, vcc, 0, v41, vcc
	global_store_dwordx2 v[76:77], v[42:43], off
	ds_read2_b32 v[42:43], v49 offset0:97 offset1:105
	ds_read2_b32 v[76:77], v49 offset0:162 offset1:170
	ds_read2_b32 v[78:79], v49 offset0:227 offset1:235
	ds_read2_b32 v[80:81], v49 offset0:32 offset1:40
	ds_read2_b32 v[82:83], v1 offset0:36 offset1:44
	ds_read2_b32 v[84:85], v1 offset0:101 offset1:109
	ds_read2_b32 v[86:87], v1 offset0:166 offset1:174
	ds_read2_b32 v[88:89], v1 offset0:231 offset1:239
	s_waitcnt lgkmcnt(4)
	v_mul_f32_e32 v75, 0x41800000, v80
	s_waitcnt lgkmcnt(3)
	v_mul_f32_e32 v80, 0x41800000, v82
	s_waitcnt lgkmcnt(2)
	v_mul_f32_e32 v82, 0x41800000, v84
	v_med3_f32 v80, v80, s87, v74
	v_med3_f32 v82, v82, s87, v74
	v_mov_b32_e32 v91, v3
	v_mul_f32_e32 v42, 0x41800000, v42
	v_cvt_pk_fp8_f32 v91, v80, v82
	v_med3_f32 v75, v75, s87, v74
	v_med3_f32 v42, v42, s87, v74
	v_mov_b32_e32 v90, v3
	s_waitcnt lgkmcnt(1)
	v_mul_f32_e32 v84, 0x41800000, v86
	v_cvt_pk_fp8_f32 v90, v75, v42
	s_waitcnt lgkmcnt(0)
	v_mul_f32_e32 v42, 0x41800000, v88
	v_med3_f32 v84, v84, s87, v74
	v_med3_f32 v42, v42, s87, v74
	v_cvt_pk_fp8_f32 v91, v84, v42 op_sel:[0,0,1]
	v_mul_f32_e32 v42, 0x41800000, v81
	v_mul_f32_e32 v76, 0x41800000, v76
	v_mul_f32_e32 v78, 0x41800000, v78
	v_med3_f32 v75, v42, s87, v74
	v_mul_f32_e32 v42, 0x41800000, v43
	v_med3_f32 v76, v76, s87, v74
	v_med3_f32 v78, v78, s87, v74
	v_med3_f32 v43, v42, s87, v74
	v_mul_f32_e32 v42, 0x41800000, v77
	v_cvt_pk_fp8_f32 v90, v76, v78 op_sel:[0,0,1]
	v_med3_f32 v76, v42, s87, v74
	v_mul_f32_e32 v42, 0x41800000, v79
	v_med3_f32 v77, v42, s87, v74
	v_mul_f32_e32 v42, 0x41800000, v83
	v_med3_f32 v78, v42, s87, v74
	v_mul_f32_e32 v42, 0x41800000, v85
	v_med3_f32 v79, v42, s87, v74
	v_mul_f32_e32 v42, 0x41800000, v87
	v_med3_f32 v80, v42, s87, v74
	v_mov_b32_e32 v42, v3
	v_cvt_pk_fp8_f32 v42, v75, v43
	v_mov_b32_e32 v43, v3
	v_cvt_pk_fp8_f32 v43, v78, v79
	v_mul_f32_e32 v75, 0x41800000, v89
	v_med3_f32 v75, v75, s87, v74
	v_add_co_u32_e32 v92, vcc, s89, v40
	v_cvt_pk_fp8_f32 v42, v76, v77 op_sel:[0,0,1]
	v_cvt_pk_fp8_f32 v43, v80, v75 op_sel:[0,0,1]
	v_addc_co_u32_e32 v93, vcc, 0, v41, vcc
	v_add_co_u32_e32 v76, vcc, s93, v40
	global_store_dwordx2 v[92:93], v[90:91], off
	s_nop 0
	v_addc_co_u32_e32 v77, vcc, 0, v41, vcc
	global_store_dwordx2 v[76:77], v[42:43], off
	ds_read2_b32 v[42:43], v49 offset0:113 offset1:121
	ds_read2_b32 v[76:77], v49 offset0:178 offset1:186
	ds_read2_b32 v[78:79], v49 offset0:243 offset1:251
	ds_read2_b32 v[80:81], v49 offset0:48 offset1:56
	ds_read2_b32 v[82:83], v1 offset0:52 offset1:60
	ds_read2_b32 v[84:85], v1 offset0:117 offset1:125
	ds_read2_b32 v[86:87], v1 offset0:182 offset1:190
	ds_read2_b32 v[88:89], v1 offset0:247 offset1:255
	s_waitcnt lgkmcnt(4)
	v_mul_f32_e32 v1, 0x41800000, v80
	v_mul_f32_e32 v42, 0x41800000, v42
	v_med3_f32 v1, v1, s87, v74
	v_med3_f32 v42, v42, s87, v74
	v_mov_b32_e32 v90, v3
	v_cvt_pk_fp8_f32 v90, v1, v42
	v_mul_f32_e32 v75, 0x41800000, v76
	v_mul_f32_e32 v76, 0x41800000, v78
	s_waitcnt lgkmcnt(3)
	v_mul_f32_e32 v78, 0x41800000, v82
	s_waitcnt lgkmcnt(2)
	v_mul_f32_e32 v80, 0x41800000, v84
	v_med3_f32 v78, v78, s87, v74
	v_med3_f32 v80, v80, s87, v74
	v_mov_b32_e32 v91, v3
	v_mul_f32_e32 v42, 0x41800000, v43
	v_med3_f32 v75, v75, s87, v74
	v_med3_f32 v76, v76, s87, v74
	v_cvt_pk_fp8_f32 v91, v78, v80
	v_med3_f32 v43, v42, s87, v74
	v_mul_f32_e32 v42, 0x41800000, v77
	v_cvt_pk_fp8_f32 v90, v75, v76 op_sel:[0,0,1]
	v_med3_f32 v75, v42, s87, v74
	v_mul_f32_e32 v42, 0x41800000, v79
	s_waitcnt lgkmcnt(1)
	v_mul_f32_e32 v82, 0x41800000, v86
	s_waitcnt lgkmcnt(0)
	v_mul_f32_e32 v1, 0x41800000, v88
	v_med3_f32 v76, v42, s87, v74
	v_mul_f32_e32 v42, 0x41800000, v83
	v_med3_f32 v82, v82, s87, v74
	v_med3_f32 v1, v1, s87, v74
	v_med3_f32 v77, v42, s87, v74
	v_mul_f32_e32 v42, 0x41800000, v85
	v_cvt_pk_fp8_f32 v91, v82, v1 op_sel:[0,0,1]
	v_mul_f32_e32 v1, 0x41800000, v81
	v_med3_f32 v78, v42, s87, v74
	v_mul_f32_e32 v42, 0x41800000, v87
	v_med3_f32 v1, v1, s87, v74
	v_med3_f32 v79, v42, s87, v74
	v_mov_b32_e32 v42, v3
	v_cvt_pk_fp8_f32 v42, v1, v43
	v_mov_b32_e32 v43, v3
	v_cvt_pk_fp8_f32 v43, v77, v78
	v_mul_f32_e32 v1, 0x41800000, v89
	v_med3_f32 v1, v1, s87, v74
	v_add_co_u32_e32 v92, vcc, s90, v40
	v_cvt_pk_fp8_f32 v42, v75, v76 op_sel:[0,0,1]
	v_cvt_pk_fp8_f32 v43, v79, v1 op_sel:[0,0,1]
	v_addc_co_u32_e32 v93, vcc, 0, v41, vcc
	v_add_co_u32_e32 v40, vcc, 0x1c000, v40
	global_store_dwordx2 v[92:93], v[90:91], off
	s_nop 0
	v_addc_co_u32_e32 v41, vcc, 0, v41, vcc
	global_store_dwordx2 v[40:41], v[42:43], off
	s_waitcnt lgkmcnt(0)

.LBB0_269:
	s_andn2_b64 vcc, exec, s[2:3]
	s_cbranch_vccnz .LBB0_34
	s_ashr_i32 s2, s75, 31
	s_lshr_b32 s2, s2, 25
	s_add_i32 s2, s75, s2
	s_ashr_i32 s8, s2, 7
	s_and_b32 s2, s2, 0xffffff80
	s_sub_i32 s4, s75, s2
	s_lshl_b32 s9, s8, 13
	s_sub_i32 s34, s95, s9
	s_add_i32 s2, s4, -16
	s_cmp_gt_u32 s2, 39
	s_mov_b64 s[2:3], -1
	s_cbranch_scc0 .LBB0_276
	s_lshl_b32 s2, s8, 6
	s_ashr_i32 s3, s2, 31
	s_lshl_b64 s[10:11], s[2:3], 15
	s_add_u32 s10, s26, s10
	s_addc_u32 s11, s27, s11
	s_cmp_lt_i32 s4, 64
	s_mov_b64 s[4:5], -1
	s_cbranch_scc0 .LBB0_273
	s_ashr_i32 s5, s34, 31
	s_mov_b32 s4, s34
	s_lshl_b64 s[64:65], s[4:5], 2
	s_add_u32 s64, s10, s64
	s_addc_u32 s65, s11, s65
	v_lshl_add_u64 v[132:133], s[64:65], 0, v[18:19]
	v_add_co_u32_e32 v76, vcc, s91, v132
	s_mov_b32 s64, 0x80000
	s_nop 0
	v_addc_co_u32_e32 v77, vcc, 0, v133, vcc
	v_add_co_u32_e32 v80, vcc, s1, v132
	global_load_dwordx4 v[40:43], v[132:133], off nt
	s_nop 0
	global_load_dwordx4 v[76:79], v[76:77], off nt
	v_addc_co_u32_e32 v81, vcc, 0, v133, vcc
	v_add_co_u32_e32 v84, vcc, s30, v132
	v_add_u32_e32 v1, 0x410, v48
	s_nop 0
	v_addc_co_u32_e32 v85, vcc, 0, v133, vcc
	global_load_dwordx4 v[80:83], v[80:81], off nt
	s_nop 0
	global_load_dwordx4 v[84:87], v[84:85], off nt
	v_add_co_u32_e32 v88, vcc, s64, v132
	s_mov_b32 s64, 0xa0000
	s_nop 0
	v_addc_co_u32_e32 v89, vcc, 0, v133, vcc
	v_add_co_u32_e32 v92, vcc, s64, v132
	s_mov_b32 s64, 0xc0000
	s_nop 0
	v_addc_co_u32_e32 v93, vcc, 0, v133, vcc
	global_load_dwordx4 v[88:91], v[88:89], off nt
	s_nop 0
	global_load_dwordx4 v[92:95], v[92:93], off nt
	v_add_co_u32_e32 v96, vcc, s64, v132
	s_mov_b32 s64, 0xe0000
	s_nop 0
	v_addc_co_u32_e32 v97, vcc, 0, v133, vcc
	v_add_co_u32_e32 v100, vcc, s64, v132
	s_mov_b32 s64, 0x100000
	s_nop 0
	v_addc_co_u32_e32 v101, vcc, 0, v133, vcc
	global_load_dwordx4 v[96:99], v[96:97], off nt
	s_nop 0
	global_load_dwordx4 v[100:103], v[100:101], off nt
	v_add_co_u32_e32 v104, vcc, s64, v132
	s_mov_b32 s64, 0x120000
	s_nop 0
	v_addc_co_u32_e32 v105, vcc, 0, v133, vcc
	v_add_co_u32_e32 v108, vcc, s64, v132
	s_mov_b32 s64, 0x140000
	s_nop 0
	v_addc_co_u32_e32 v109, vcc, 0, v133, vcc
	global_load_dwordx4 v[104:107], v[104:105], off nt
	s_nop 0
	global_load_dwordx4 v[108:111], v[108:109], off nt
	v_add_co_u32_e32 v112, vcc, s64, v132
	s_mov_b32 s64, 0x160000
	s_nop 0
	v_addc_co_u32_e32 v113, vcc, 0, v133, vcc
	v_add_co_u32_e32 v116, vcc, s64, v132
	s_mov_b32 s64, 0x180000
	s_nop 0
	v_addc_co_u32_e32 v117, vcc, 0, v133, vcc
	global_load_dwordx4 v[112:115], v[112:113], off nt
	s_nop 0
	global_load_dwordx4 v[116:119], v[116:117], off nt
	v_add_co_u32_e32 v120, vcc, s64, v132
	s_mov_b32 s64, 0x1a0000
	s_nop 0
	v_addc_co_u32_e32 v121, vcc, 0, v133, vcc
	v_add_co_u32_e32 v124, vcc, s64, v132
	s_mov_b32 s64, 0x1c0000
	s_nop 0
	v_addc_co_u32_e32 v125, vcc, 0, v133, vcc
	global_load_dwordx4 v[120:123], v[120:121], off nt
	s_nop 0
	global_load_dwordx4 v[124:127], v[124:125], off nt
	v_add_co_u32_e32 v128, vcc, s64, v132
	s_mov_b32 s64, 0x1e0000
	s_nop 0
	v_addc_co_u32_e32 v129, vcc, 0, v133, vcc
	global_load_dwordx4 v[128:131], v[128:129], off nt
	v_add_co_u32_e32 v132, vcc, s64, v132
	s_lshl_b64 s[4:5], s[4:5], 11
	s_nop 0
	v_addc_co_u32_e32 v133, vcc, 0, v133, vcc
	global_load_dwordx4 v[132:135], v[132:133], off nt
	s_waitcnt vmcnt(15)
	ds_write2_b32 v48, v40, v41 offset1:1
	ds_write2_b32 v48, v42, v43 offset0:2 offset1:3
	s_waitcnt vmcnt(14)
	ds_write2_b32 v1, v76, v77 offset1:1
	v_add_u32_e32 v1, 0x418, v48
	ds_write2_b32 v1, v78, v79 offset1:1
	v_add_u32_e32 v1, 0x820, v48
	s_add_u32 s4, s84, s4
	s_addc_u32 s5, s85, s5
	s_add_u32 s4, s4, s2
	s_waitcnt vmcnt(13)
	ds_write2_b32 v1, v80, v81 offset1:1
	v_add_u32_e32 v1, 0x828, v48
	ds_write2_b32 v1, v82, v83 offset1:1
	v_add_u32_e32 v1, 0xc30, v48
	s_waitcnt vmcnt(12)
	ds_write2_b32 v1, v84, v85 offset1:1
	v_add_u32_e32 v1, 0xc38, v48
	ds_write2_b32 v1, v86, v87 offset1:1
	v_add_u32_e32 v1, 0x1040, v48
	s_addc_u32 s5, s5, s3
	s_waitcnt vmcnt(11)
	ds_write2_b32 v1, v88, v89 offset1:1
	v_add_u32_e32 v1, 0x1048, v48
	ds_write2_b32 v1, v90, v91 offset1:1
	v_add_u32_e32 v1, 0x1450, v48
	s_waitcnt vmcnt(10)
	ds_write2_b32 v1, v92, v93 offset1:1
	v_add_u32_e32 v1, 0x1458, v48
	ds_write2_b32 v1, v94, v95 offset1:1
	v_add_u32_e32 v1, 0x1860, v48
	v_mov_b32_e32 v90, v3
	v_mov_b32_e32 v91, v3
	s_waitcnt vmcnt(9)
	ds_write2_b32 v1, v96, v97 offset1:1
	v_add_u32_e32 v1, 0x1868, v48
	ds_write2_b32 v1, v98, v99 offset1:1
	v_add_u32_e32 v1, 0x1c70, v48
	s_waitcnt vmcnt(8)
	ds_write2_b32 v1, v100, v101 offset1:1
	v_add_u32_e32 v1, 0x1c78, v48
	ds_write2_b32 v1, v102, v103 offset1:1
	v_add_u32_e32 v1, 0x2080, v48
	s_waitcnt vmcnt(7)
	ds_write2_b32 v1, v104, v105 offset1:1
	v_add_u32_e32 v1, 0x2088, v48
	ds_write2_b32 v1, v106, v107 offset1:1
	v_add_u32_e32 v1, 0x2490, v48
	s_waitcnt vmcnt(6)
	ds_write2_b32 v1, v108, v109 offset1:1
	v_add_u32_e32 v1, 0x2498, v48
	ds_write2_b32 v1, v110, v111 offset1:1
	v_add_u32_e32 v1, 0x28a0, v48
	s_waitcnt vmcnt(5)
	ds_write2_b32 v1, v112, v113 offset1:1
	v_add_u32_e32 v1, 0x28a8, v48
	ds_write2_b32 v1, v114, v115 offset1:1
	v_add_u32_e32 v1, 0x2cb0, v48
	s_waitcnt vmcnt(4)
	ds_write2_b32 v1, v116, v117 offset1:1
	v_add_u32_e32 v1, 0x2cb8, v48
	ds_write2_b32 v1, v118, v119 offset1:1
	v_add_u32_e32 v1, 0x30c0, v48
	s_waitcnt vmcnt(3)
	ds_write2_b32 v1, v120, v121 offset1:1
	v_add_u32_e32 v1, 0x30c8, v48
	ds_write2_b32 v1, v122, v123 offset1:1
	v_add_u32_e32 v1, 0x34d0, v48
	s_waitcnt vmcnt(2)
	ds_write2_b32 v1, v124, v125 offset1:1
	v_add_u32_e32 v1, 0x34d8, v48
	ds_write2_b32 v1, v126, v127 offset1:1
	v_add_u32_e32 v1, 0x38e0, v48
	s_waitcnt vmcnt(1)
	ds_write2_b32 v1, v128, v129 offset1:1
	v_add_u32_e32 v1, 0x38e8, v48
	ds_write2_b32 v1, v130, v131 offset1:1
	v_add_u32_e32 v1, 0x3cf0, v48
	s_waitcnt vmcnt(0)
	ds_write2_b32 v1, v132, v133 offset1:1
	v_add_u32_e32 v1, 0x3cf8, v48
	ds_write2_b32 v1, v134, v135 offset1:1
	s_waitcnt lgkmcnt(0)
	ds_read2_b32 v[42:43], v49 offset0:65 offset1:73
	ds_read2_b32 v[76:77], v49 offset0:130 offset1:138
	ds_read2_b32 v[78:79], v49 offset0:195 offset1:203
	v_add_u32_e32 v1, 0x400, v49
	ds_read2_b32 v[80:81], v49 offset1:8
	ds_read2_b32 v[82:83], v1 offset0:4 offset1:12
	ds_read2_b32 v[84:85], v1 offset0:69 offset1:77
	ds_read2_b32 v[86:87], v1 offset0:134 offset1:142
	ds_read2_b32 v[88:89], v1 offset0:199 offset1:207
	s_waitcnt lgkmcnt(4)
	v_mul_f32_e32 v40, 0x41800000, v80
	v_mul_f32_e32 v41, 0x41800000, v42
	v_med3_f32 v40, v40, s87, v74
	v_med3_f32 v41, v41, s87, v74
	v_cvt_pk_fp8_f32 v90, v40, v41
	v_mul_f32_e32 v42, 0x41800000, v76
	v_mul_f32_e32 v75, 0x41800000, v78
	v_med3_f32 v42, v42, s87, v74
	v_med3_f32 v75, v75, s87, v74
	v_cvt_pk_fp8_f32 v90, v42, v75 op_sel:[0,0,1]
	v_mul_f32_e32 v42, 0x41800000, v81
	s_waitcnt lgkmcnt(3)
	v_mul_f32_e32 v76, 0x41800000, v82
	s_waitcnt lgkmcnt(2)
	v_mul_f32_e32 v78, 0x41800000, v84
	v_med3_f32 v75, v42, s87, v74
	v_mul_f32_e32 v42, 0x41800000, v43
	v_med3_f32 v76, v76, s87, v74
	v_med3_f32 v78, v78, s87, v74
	v_med3_f32 v43, v42, s87, v74
	v_mul_f32_e32 v42, 0x41800000, v77
	v_cvt_pk_fp8_f32 v91, v76, v78
	v_med3_f32 v76, v42, s87, v74
	v_mul_f32_e32 v42, 0x41800000, v79
	v_med3_f32 v77, v42, s87, v74
	v_mul_f32_e32 v42, 0x41800000, v83
	s_waitcnt lgkmcnt(1)
	v_mul_f32_e32 v80, 0x41800000, v86
	s_waitcnt lgkmcnt(0)
	v_mul_f32_e32 v40, 0x41800000, v88
	v_med3_f32 v78, v42, s87, v74
	v_mul_f32_e32 v42, 0x41800000, v85
	v_med3_f32 v80, v80, s87, v74
	v_med3_f32 v40, v40, s87, v74
	v_med3_f32 v79, v42, s87, v74
	v_mul_f32_e32 v42, 0x41800000, v87
	v_cvt_pk_fp8_f32 v91, v80, v40 op_sel:[0,0,1]
	v_med3_f32 v80, v42, s87, v74
	v_mov_b32_e32 v42, v3
	v_cvt_pk_fp8_f32 v42, v75, v43
	v_mov_b32_e32 v43, v3
	v_cvt_pk_fp8_f32 v43, v78, v79
	v_mul_f32_e32 v75, 0x41800000, v89
	v_med3_f32 v75, v75, s87, v74
	v_cvt_pk_fp8_f32 v42, v76, v77 op_sel:[0,0,1]
	v_cvt_pk_fp8_f32 v43, v80, v75 op_sel:[0,0,1]
	v_lshl_add_u64 v[40:41], s[4:5], 0, v[16:17]
	v_add_co_u32_e32 v76, vcc, s68, v40
	global_store_dwordx2 v[40:41], v[90:91], off
	s_nop 0
	v_addc_co_u32_e32 v77, vcc, 0, v41, vcc
	global_store_dwordx2 v[76:77], v[42:43], off
	ds_read2_b32 v[42:43], v49 offset0:81 offset1:89
	ds_read2_b32 v[76:77], v49 offset0:146 offset1:154
	ds_read2_b32 v[78:79], v49 offset0:211 offset1:219
	ds_read2_b32 v[80:81], v49 offset0:16 offset1:24
	ds_read2_b32 v[82:83], v1 offset0:20 offset1:28
	ds_read2_b32 v[84:85], v1 offset0:85 offset1:93
	ds_read2_b32 v[86:87], v1 offset0:150 offset1:158
	ds_read2_b32 v[88:89], v1 offset0:215 offset1:223
	s_waitcnt lgkmcnt(4)
	v_mul_f32_e32 v75, 0x41800000, v80
	s_waitcnt lgkmcnt(3)
	v_mul_f32_e32 v80, 0x41800000, v82
	s_waitcnt lgkmcnt(2)
	v_mul_f32_e32 v82, 0x41800000, v84
	v_med3_f32 v80, v80, s87, v74
	v_med3_f32 v82, v82, s87, v74
	v_mov_b32_e32 v91, v3
	v_mul_f32_e32 v42, 0x41800000, v42
	v_cvt_pk_fp8_f32 v91, v80, v82
	v_med3_f32 v75, v75, s87, v74
	v_med3_f32 v42, v42, s87, v74
	v_mov_b32_e32 v90, v3
	s_waitcnt lgkmcnt(1)
	v_mul_f32_e32 v84, 0x41800000, v86
	v_cvt_pk_fp8_f32 v90, v75, v42
	s_waitcnt lgkmcnt(0)
	v_mul_f32_e32 v42, 0x41800000, v88
	v_med3_f32 v84, v84, s87, v74
	v_med3_f32 v42, v42, s87, v74
	v_cvt_pk_fp8_f32 v91, v84, v42 op_sel:[0,0,1]
	v_mul_f32_e32 v42, 0x41800000, v81
	v_mul_f32_e32 v76, 0x41800000, v76
	v_mul_f32_e32 v78, 0x41800000, v78
	v_med3_f32 v75, v42, s87, v74
	v_mul_f32_e32 v42, 0x41800000, v43
	v_med3_f32 v76, v76, s87, v74
	v_med3_f32 v78, v78, s87, v74
	v_med3_f32 v43, v42, s87, v74
	v_mul_f32_e32 v42, 0x41800000, v77
	v_cvt_pk_fp8_f32 v90, v76, v78 op_sel:[0,0,1]
	v_med3_f32 v76, v42, s87, v74
	v_mul_f32_e32 v42, 0x41800000, v79
	v_med3_f32 v77, v42, s87, v74
	v_mul_f32_e32 v42, 0x41800000, v83
	v_med3_f32 v78, v42, s87, v74
	v_mul_f32_e32 v42, 0x41800000, v85
	v_med3_f32 v79, v42, s87, v74
	v_mul_f32_e32 v42, 0x41800000, v87
	v_med3_f32 v80, v42, s87, v74
	v_mov_b32_e32 v42, v3
	v_cvt_pk_fp8_f32 v42, v75, v43
	v_mov_b32_e32 v43, v3
	v_cvt_pk_fp8_f32 v43, v78, v79
	v_mul_f32_e32 v75, 0x41800000, v89
	v_med3_f32 v75, v75, s87, v74
	v_add_co_u32_e32 v92, vcc, s88, v40
	v_cvt_pk_fp8_f32 v42, v76, v77 op_sel:[0,0,1]
	v_cvt_pk_fp8_f32 v43, v80, v75 op_sel:[0,0,1]
	v_addc_co_u32_e32 v93, vcc, 0, v41, vcc
	v_add_co_u32_e32 v76, vcc, s92, v40
	global_store_dwordx2 v[92:93], v[90:91], off
	s_nop 0
	v_addc_co_u32_e32 v77, vcc, 0, v41, vcc
	global_store_dwordx2 v[76:77], v[42:43], off
	ds_read2_b32 v[42:43], v49 offset0:97 offset1:105
	ds_read2_b32 v[76:77], v49 offset0:162 offset1:170
	ds_read2_b32 v[78:79], v49 offset0:227 offset1:235
	ds_read2_b32 v[80:81], v49 offset0:32 offset1:40
	ds_read2_b32 v[82:83], v1 offset0:36 offset1:44
	ds_read2_b32 v[84:85], v1 offset0:101 offset1:109
	ds_read2_b32 v[86:87], v1 offset0:166 offset1:174
	ds_read2_b32 v[88:89], v1 offset0:231 offset1:239
	s_waitcnt lgkmcnt(4)
	v_mul_f32_e32 v75, 0x41800000, v80
	s_waitcnt lgkmcnt(3)
	v_mul_f32_e32 v80, 0x41800000, v82
	s_waitcnt lgkmcnt(2)
	v_mul_f32_e32 v82, 0x41800000, v84
	v_med3_f32 v80, v80, s87, v74
	v_med3_f32 v82, v82, s87, v74
	v_mov_b32_e32 v91, v3
	v_mul_f32_e32 v42, 0x41800000, v42
	v_cvt_pk_fp8_f32 v91, v80, v82
	v_med3_f32 v75, v75, s87, v74
	v_med3_f32 v42, v42, s87, v74
	v_mov_b32_e32 v90, v3
	s_waitcnt lgkmcnt(1)
	v_mul_f32_e32 v84, 0x41800000, v86
	v_cvt_pk_fp8_f32 v90, v75, v42
	s_waitcnt lgkmcnt(0)
	v_mul_f32_e32 v42, 0x41800000, v88
	v_med3_f32 v84, v84, s87, v74
	v_med3_f32 v42, v42, s87, v74
	v_cvt_pk_fp8_f32 v91, v84, v42 op_sel:[0,0,1]
	v_mul_f32_e32 v42, 0x41800000, v81
	v_mul_f32_e32 v76, 0x41800000, v76
	v_mul_f32_e32 v78, 0x41800000, v78
	v_med3_f32 v75, v42, s87, v74
	v_mul_f32_e32 v42, 0x41800000, v43
	v_med3_f32 v76, v76, s87, v74
	v_med3_f32 v78, v78, s87, v74
	v_med3_f32 v43, v42, s87, v74
	v_mul_f32_e32 v42, 0x41800000, v77
	v_cvt_pk_fp8_f32 v90, v76, v78 op_sel:[0,0,1]
	v_med3_f32 v76, v42, s87, v74
	v_mul_f32_e32 v42, 0x41800000, v79
	v_med3_f32 v77, v42, s87, v74
	v_mul_f32_e32 v42, 0x41800000, v83
	v_med3_f32 v78, v42, s87, v74
	v_mul_f32_e32 v42, 0x41800000, v85
	v_med3_f32 v79, v42, s87, v74
	v_mul_f32_e32 v42, 0x41800000, v87
	v_med3_f32 v80, v42, s87, v74
	v_mov_b32_e32 v42, v3
	v_cvt_pk_fp8_f32 v42, v75, v43
	v_mov_b32_e32 v43, v3
	v_cvt_pk_fp8_f32 v43, v78, v79
	v_mul_f32_e32 v75, 0x41800000, v89
	v_med3_f32 v75, v75, s87, v74
	v_add_co_u32_e32 v92, vcc, s89, v40
	v_cvt_pk_fp8_f32 v42, v76, v77 op_sel:[0,0,1]
	v_cvt_pk_fp8_f32 v43, v80, v75 op_sel:[0,0,1]
	v_addc_co_u32_e32 v93, vcc, 0, v41, vcc
	v_add_co_u32_e32 v76, vcc, s93, v40
	global_store_dwordx2 v[92:93], v[90:91], off
	s_nop 0
	v_addc_co_u32_e32 v77, vcc, 0, v41, vcc
	global_store_dwordx2 v[76:77], v[42:43], off
	ds_read2_b32 v[42:43], v49 offset0:113 offset1:121
	ds_read2_b32 v[76:77], v49 offset0:178 offset1:186
	ds_read2_b32 v[78:79], v49 offset0:243 offset1:251
	ds_read2_b32 v[80:81], v49 offset0:48 offset1:56
	ds_read2_b32 v[82:83], v1 offset0:52 offset1:60
	ds_read2_b32 v[84:85], v1 offset0:117 offset1:125
	ds_read2_b32 v[86:87], v1 offset0:182 offset1:190
	ds_read2_b32 v[88:89], v1 offset0:247 offset1:255
	s_waitcnt lgkmcnt(4)
	v_mul_f32_e32 v1, 0x41800000, v80
	v_mul_f32_e32 v42, 0x41800000, v42
	v_med3_f32 v1, v1, s87, v74
	v_med3_f32 v42, v42, s87, v74
	v_mov_b32_e32 v90, v3
	v_cvt_pk_fp8_f32 v90, v1, v42
	v_mul_f32_e32 v75, 0x41800000, v76
	v_mul_f32_e32 v76, 0x41800000, v78
	s_waitcnt lgkmcnt(3)
	v_mul_f32_e32 v78, 0x41800000, v82
	s_waitcnt lgkmcnt(2)
	v_mul_f32_e32 v80, 0x41800000, v84
	v_med3_f32 v78, v78, s87, v74
	v_med3_f32 v80, v80, s87, v74
	v_mov_b32_e32 v91, v3
	v_mul_f32_e32 v42, 0x41800000, v43
	v_med3_f32 v75, v75, s87, v74
	v_med3_f32 v76, v76, s87, v74
	v_cvt_pk_fp8_f32 v91, v78, v80
	v_med3_f32 v43, v42, s87, v74
	v_mul_f32_e32 v42, 0x41800000, v77
	v_cvt_pk_fp8_f32 v90, v75, v76 op_sel:[0,0,1]
	v_med3_f32 v75, v42, s87, v74
	v_mul_f32_e32 v42, 0x41800000, v79
	s_waitcnt lgkmcnt(1)
	v_mul_f32_e32 v82, 0x41800000, v86
	s_waitcnt lgkmcnt(0)
	v_mul_f32_e32 v1, 0x41800000, v88
	v_med3_f32 v76, v42, s87, v74
	v_mul_f32_e32 v42, 0x41800000, v83
	v_med3_f32 v82, v82, s87, v74
	v_med3_f32 v1, v1, s87, v74
	v_med3_f32 v77, v42, s87, v74
	v_mul_f32_e32 v42, 0x41800000, v85
	v_cvt_pk_fp8_f32 v91, v82, v1 op_sel:[0,0,1]
	v_mul_f32_e32 v1, 0x41800000, v81
	v_med3_f32 v78, v42, s87, v74
	v_mul_f32_e32 v42, 0x41800000, v87
	v_med3_f32 v1, v1, s87, v74
	v_med3_f32 v79, v42, s87, v74
	v_mov_b32_e32 v42, v3
	v_cvt_pk_fp8_f32 v42, v1, v43
	v_mov_b32_e32 v43, v3
	v_cvt_pk_fp8_f32 v43, v77, v78
	v_mul_f32_e32 v1, 0x41800000, v89
	v_med3_f32 v1, v1, s87, v74
	v_add_co_u32_e32 v92, vcc, s90, v40
	v_cvt_pk_fp8_f32 v42, v75, v76 op_sel:[0,0,1]
	v_cvt_pk_fp8_f32 v43, v79, v1 op_sel:[0,0,1]
	v_addc_co_u32_e32 v93, vcc, 0, v41, vcc
	v_add_co_u32_e32 v40, vcc, 0x1c000, v40
	global_store_dwordx2 v[92:93], v[90:91], off
	s_nop 0
	v_addc_co_u32_e32 v41, vcc, 0, v41, vcc
	global_store_dwordx2 v[40:41], v[42:43], off
	s_waitcnt lgkmcnt(0)
	s_mov_b64 s[4:5], 0
.LBB0_273:
	s_andn2_b64 vcc, exec, s[4:5]
	s_cbranch_vccnz .LBB0_275
	s_lshl_b64 s[4:5], s[34:35], 2
	s_add_u32 s4, s10, s4
	s_addc_u32 s5, s11, s5
	v_lshl_add_u64 v[132:133], s[4:5], 0, v[18:19]
	v_add_co_u32_e32 v76, vcc, 0x20000, v132
	v_add_u32_e32 v1, 0x410, v48
	s_nop 0
	v_addc_co_u32_e32 v77, vcc, 0, v133, vcc
	v_add_co_u32_e32 v80, vcc, 0x40000, v132
	global_load_dwordx4 v[40:43], v[132:133], off nt
	s_nop 0
	global_load_dwordx4 v[76:79], v[76:77], off nt
	v_addc_co_u32_e32 v81, vcc, 0, v133, vcc
	v_add_co_u32_e32 v84, vcc, 0x60000, v132
	s_add_i32 s4, s34, 0xfffff000
	s_nop 0
	v_addc_co_u32_e32 v85, vcc, 0, v133, vcc
	global_load_dwordx4 v[80:83], v[80:81], off nt
	s_nop 0
	global_load_dwordx4 v[84:87], v[84:85], off nt
	v_add_co_u32_e32 v88, vcc, 0x80000, v132
	s_mov_b32 s5, s35
	s_nop 0
	v_addc_co_u32_e32 v89, vcc, 0, v133, vcc
	v_add_co_u32_e32 v92, vcc, 0xa0000, v132
	s_lshl_b64 s[4:5], s[4:5], 11
	s_nop 0
	v_addc_co_u32_e32 v93, vcc, 0, v133, vcc
	global_load_dwordx4 v[88:91], v[88:89], off nt
	s_nop 0
	global_load_dwordx4 v[92:95], v[92:93], off nt
	v_add_co_u32_e32 v96, vcc, 0xc0000, v132
	v_readlane_b32 s10, v255, 23
	s_nop 0
	v_addc_co_u32_e32 v97, vcc, 0, v133, vcc
	v_add_co_u32_e32 v100, vcc, 0xe0000, v132
	s_add_u32 s4, s10, s4
	s_nop 0
	v_addc_co_u32_e32 v101, vcc, 0, v133, vcc
	global_load_dwordx4 v[96:99], v[96:97], off nt
	s_nop 0
	global_load_dwordx4 v[100:103], v[100:101], off nt
	v_add_co_u32_e32 v104, vcc, 0x100000, v132
	v_readlane_b32 s10, v255, 25
	s_nop 0
	v_addc_co_u32_e32 v105, vcc, 0, v133, vcc
	v_add_co_u32_e32 v108, vcc, 0x120000, v132
	s_addc_u32 s5, s10, s5
	s_nop 0
	v_addc_co_u32_e32 v109, vcc, 0, v133, vcc
	global_load_dwordx4 v[104:107], v[104:105], off nt
	s_nop 0
	global_load_dwordx4 v[108:111], v[108:109], off nt
	v_add_co_u32_e32 v112, vcc, 0x140000, v132
	s_add_u32 s2, s4, s2
	s_nop 0
	v_addc_co_u32_e32 v113, vcc, 0, v133, vcc
	v_add_co_u32_e32 v116, vcc, 0x160000, v132
	s_addc_u32 s3, s5, s3
	s_nop 0
	v_addc_co_u32_e32 v117, vcc, 0, v133, vcc
	global_load_dwordx4 v[112:115], v[112:113], off nt
	s_nop 0
	global_load_dwordx4 v[116:119], v[116:117], off nt
	v_add_co_u32_e32 v120, vcc, 0x180000, v132
	s_nop 1
	v_addc_co_u32_e32 v121, vcc, 0, v133, vcc
	v_add_co_u32_e32 v124, vcc, 0x1a0000, v132
	s_nop 1
	v_addc_co_u32_e32 v125, vcc, 0, v133, vcc
	global_load_dwordx4 v[120:123], v[120:121], off nt
	s_nop 0
	global_load_dwordx4 v[124:127], v[124:125], off nt
	v_add_co_u32_e32 v128, vcc, 0x1c0000, v132
	s_nop 1
	v_addc_co_u32_e32 v129, vcc, 0, v133, vcc
	global_load_dwordx4 v[128:131], v[128:129], off nt
	v_add_co_u32_e32 v132, vcc, 0x1e0000, v132
	s_nop 1
	v_addc_co_u32_e32 v133, vcc, 0, v133, vcc
	global_load_dwordx4 v[132:135], v[132:133], off nt
	s_waitcnt vmcnt(15)
	ds_write2_b32 v48, v40, v41 offset1:1
	ds_write2_b32 v48, v42, v43 offset0:2 offset1:3
	s_waitcnt vmcnt(14)
	ds_write2_b32 v1, v76, v77 offset1:1
	v_add_u32_e32 v1, 0x418, v48
	ds_write2_b32 v1, v78, v79 offset1:1
	v_add_u32_e32 v1, 0x820, v48
	s_waitcnt vmcnt(13)
	ds_write2_b32 v1, v80, v81 offset1:1
	v_add_u32_e32 v1, 0x828, v48
	ds_write2_b32 v1, v82, v83 offset1:1
	v_add_u32_e32 v1, 0xc30, v48
	s_waitcnt vmcnt(12)
	ds_write2_b32 v1, v84, v85 offset1:1
	v_add_u32_e32 v1, 0xc38, v48
	ds_write2_b32 v1, v86, v87 offset1:1
	v_add_u32_e32 v1, 0x1040, v48
	s_waitcnt vmcnt(11)
	ds_write2_b32 v1, v88, v89 offset1:1
	v_add_u32_e32 v1, 0x1048, v48
	ds_write2_b32 v1, v90, v91 offset1:1
	v_add_u32_e32 v1, 0x1450, v48
	s_waitcnt vmcnt(10)
	ds_write2_b32 v1, v92, v93 offset1:1
	v_add_u32_e32 v1, 0x1458, v48
	ds_write2_b32 v1, v94, v95 offset1:1
	v_add_u32_e32 v1, 0x1860, v48
	v_mov_b32_e32 v90, v3
	v_mov_b32_e32 v91, v3
	s_waitcnt vmcnt(9)
	ds_write2_b32 v1, v96, v97 offset1:1
	v_add_u32_e32 v1, 0x1868, v48
	ds_write2_b32 v1, v98, v99 offset1:1
	v_add_u32_e32 v1, 0x1c70, v48
	s_waitcnt vmcnt(8)
	ds_write2_b32 v1, v100, v101 offset1:1
	v_add_u32_e32 v1, 0x1c78, v48
	ds_write2_b32 v1, v102, v103 offset1:1
	v_add_u32_e32 v1, 0x2080, v48
	s_waitcnt vmcnt(7)
	ds_write2_b32 v1, v104, v105 offset1:1
	v_add_u32_e32 v1, 0x2088, v48
	ds_write2_b32 v1, v106, v107 offset1:1
	v_add_u32_e32 v1, 0x2490, v48
	s_waitcnt vmcnt(6)
	ds_write2_b32 v1, v108, v109 offset1:1
	v_add_u32_e32 v1, 0x2498, v48
	ds_write2_b32 v1, v110, v111 offset1:1
	v_add_u32_e32 v1, 0x28a0, v48
	s_waitcnt vmcnt(5)
	ds_write2_b32 v1, v112, v113 offset1:1
	v_add_u32_e32 v1, 0x28a8, v48
	ds_write2_b32 v1, v114, v115 offset1:1
	v_add_u32_e32 v1, 0x2cb0, v48
	s_waitcnt vmcnt(4)
	ds_write2_b32 v1, v116, v117 offset1:1
	v_add_u32_e32 v1, 0x2cb8, v48
	ds_write2_b32 v1, v118, v119 offset1:1
	v_add_u32_e32 v1, 0x30c0, v48
	s_waitcnt vmcnt(3)
	ds_write2_b32 v1, v120, v121 offset1:1
	v_add_u32_e32 v1, 0x30c8, v48
	ds_write2_b32 v1, v122, v123 offset1:1
	v_add_u32_e32 v1, 0x34d0, v48
	s_waitcnt vmcnt(2)
	ds_write2_b32 v1, v124, v125 offset1:1
	v_add_u32_e32 v1, 0x34d8, v48
	ds_write2_b32 v1, v126, v127 offset1:1
	v_add_u32_e32 v1, 0x38e0, v48
	s_waitcnt vmcnt(1)
	ds_write2_b32 v1, v128, v129 offset1:1
	v_add_u32_e32 v1, 0x38e8, v48
	ds_write2_b32 v1, v130, v131 offset1:1
	v_add_u32_e32 v1, 0x3cf0, v48
	s_waitcnt vmcnt(0)
	ds_write2_b32 v1, v132, v133 offset1:1
	v_add_u32_e32 v1, 0x3cf8, v48
	ds_write2_b32 v1, v134, v135 offset1:1
	s_waitcnt lgkmcnt(0)
	ds_read2_b32 v[42:43], v49 offset0:65 offset1:73
	ds_read2_b32 v[76:77], v49 offset0:130 offset1:138
	ds_read2_b32 v[78:79], v49 offset0:195 offset1:203
	v_add_u32_e32 v1, 0x400, v49
	ds_read2_b32 v[80:81], v49 offset1:8
	ds_read2_b32 v[82:83], v1 offset0:4 offset1:12
	ds_read2_b32 v[84:85], v1 offset0:69 offset1:77
	ds_read2_b32 v[86:87], v1 offset0:134 offset1:142
	ds_read2_b32 v[88:89], v1 offset0:199 offset1:207
	s_waitcnt lgkmcnt(4)
	v_mul_f32_e32 v40, 0x41800000, v80
	v_mul_f32_e32 v41, 0x41800000, v42
	v_med3_f32 v40, v40, s87, v74
	v_med3_f32 v41, v41, s87, v74
	v_cvt_pk_fp8_f32 v90, v40, v41
	v_mul_f32_e32 v42, 0x41800000, v76
	v_mul_f32_e32 v75, 0x41800000, v78
	v_med3_f32 v42, v42, s87, v74
	v_med3_f32 v75, v75, s87, v74
	v_cvt_pk_fp8_f32 v90, v42, v75 op_sel:[0,0,1]
	v_mul_f32_e32 v42, 0x41800000, v81
	s_waitcnt lgkmcnt(3)
	v_mul_f32_e32 v76, 0x41800000, v82
	s_waitcnt lgkmcnt(2)
	v_mul_f32_e32 v78, 0x41800000, v84
	v_med3_f32 v75, v42, s87, v74
	v_mul_f32_e32 v42, 0x41800000, v43
	v_med3_f32 v76, v76, s87, v74
	v_med3_f32 v78, v78, s87, v74
	v_med3_f32 v43, v42, s87, v74
	v_mul_f32_e32 v42, 0x41800000, v77
	v_cvt_pk_fp8_f32 v91, v76, v78
	v_med3_f32 v76, v42, s87, v74
	v_mul_f32_e32 v42, 0x41800000, v79
	v_med3_f32 v77, v42, s87, v74
	v_mul_f32_e32 v42, 0x41800000, v83
	s_waitcnt lgkmcnt(1)
	v_mul_f32_e32 v80, 0x41800000, v86
	s_waitcnt lgkmcnt(0)
	v_mul_f32_e32 v40, 0x41800000, v88
	v_med3_f32 v78, v42, s87, v74
	v_mul_f32_e32 v42, 0x41800000, v85
	v_med3_f32 v80, v80, s87, v74
	v_med3_f32 v40, v40, s87, v74
	v_med3_f32 v79, v42, s87, v74
	v_mul_f32_e32 v42, 0x41800000, v87
	v_cvt_pk_fp8_f32 v91, v80, v40 op_sel:[0,0,1]
	v_med3_f32 v80, v42, s87, v74
	v_mov_b32_e32 v42, v3
	v_cvt_pk_fp8_f32 v42, v75, v43
	v_mov_b32_e32 v43, v3
	v_cvt_pk_fp8_f32 v43, v78, v79
	v_mul_f32_e32 v75, 0x41800000, v89
	v_med3_f32 v75, v75, s87, v74
	v_cvt_pk_fp8_f32 v42, v76, v77 op_sel:[0,0,1]
	v_cvt_pk_fp8_f32 v43, v80, v75 op_sel:[0,0,1]
	v_lshl_add_u64 v[40:41], s[2:3], 0, v[16:17]
	v_add_co_u32_e32 v76, vcc, s68, v40
	global_store_dwordx2 v[40:41], v[90:91], off
	s_nop 0
	v_addc_co_u32_e32 v77, vcc, 0, v41, vcc
	global_store_dwordx2 v[76:77], v[42:43], off
	ds_read2_b32 v[42:43], v49 offset0:81 offset1:89
	ds_read2_b32 v[76:77], v49 offset0:146 offset1:154
	ds_read2_b32 v[78:79], v49 offset0:211 offset1:219
	ds_read2_b32 v[80:81], v49 offset0:16 offset1:24
	ds_read2_b32 v[82:83], v1 offset0:20 offset1:28
	ds_read2_b32 v[84:85], v1 offset0:85 offset1:93
	ds_read2_b32 v[86:87], v1 offset0:150 offset1:158
	ds_read2_b32 v[88:89], v1 offset0:215 offset1:223
	s_waitcnt lgkmcnt(4)
	v_mul_f32_e32 v75, 0x41800000, v80
	s_waitcnt lgkmcnt(3)
	v_mul_f32_e32 v80, 0x41800000, v82
	s_waitcnt lgkmcnt(2)
	v_mul_f32_e32 v82, 0x41800000, v84
	v_med3_f32 v80, v80, s87, v74
	v_med3_f32 v82, v82, s87, v74
	v_mov_b32_e32 v91, v3
	v_mul_f32_e32 v42, 0x41800000, v42
	v_cvt_pk_fp8_f32 v91, v80, v82
	v_med3_f32 v75, v75, s87, v74
	v_med3_f32 v42, v42, s87, v74
	v_mov_b32_e32 v90, v3
	s_waitcnt lgkmcnt(1)
	v_mul_f32_e32 v84, 0x41800000, v86
	v_cvt_pk_fp8_f32 v90, v75, v42
	s_waitcnt lgkmcnt(0)
	v_mul_f32_e32 v42, 0x41800000, v88
	v_med3_f32 v84, v84, s87, v74
	v_med3_f32 v42, v42, s87, v74
	v_cvt_pk_fp8_f32 v91, v84, v42 op_sel:[0,0,1]
	v_mul_f32_e32 v42, 0x41800000, v81
	v_mul_f32_e32 v76, 0x41800000, v76
	v_mul_f32_e32 v78, 0x41800000, v78
	v_med3_f32 v75, v42, s87, v74
	v_mul_f32_e32 v42, 0x41800000, v43
	v_med3_f32 v76, v76, s87, v74
	v_med3_f32 v78, v78, s87, v74
	v_med3_f32 v43, v42, s87, v74
	v_mul_f32_e32 v42, 0x41800000, v77
	v_cvt_pk_fp8_f32 v90, v76, v78 op_sel:[0,0,1]
	v_med3_f32 v76, v42, s87, v74
	v_mul_f32_e32 v42, 0x41800000, v79
	v_med3_f32 v77, v42, s87, v74
	v_mul_f32_e32 v42, 0x41800000, v83
	v_med3_f32 v78, v42, s87, v74
	v_mul_f32_e32 v42, 0x41800000, v85
	v_med3_f32 v79, v42, s87, v74
	v_mul_f32_e32 v42, 0x41800000, v87
	v_med3_f32 v80, v42, s87, v74
	v_mov_b32_e32 v42, v3
	v_cvt_pk_fp8_f32 v42, v75, v43
	v_mov_b32_e32 v43, v3
	v_cvt_pk_fp8_f32 v43, v78, v79
	v_mul_f32_e32 v75, 0x41800000, v89
	v_med3_f32 v75, v75, s87, v74
	v_add_co_u32_e32 v92, vcc, s88, v40
	v_cvt_pk_fp8_f32 v42, v76, v77 op_sel:[0,0,1]
	v_cvt_pk_fp8_f32 v43, v80, v75 op_sel:[0,0,1]
	v_addc_co_u32_e32 v93, vcc, 0, v41, vcc
	v_add_co_u32_e32 v76, vcc, s92, v40
	global_store_dwordx2 v[92:93], v[90:91], off
	s_nop 0
	v_addc_co_u32_e32 v77, vcc, 0, v41, vcc
	global_store_dwordx2 v[76:77], v[42:43], off
	ds_read2_b32 v[42:43], v49 offset0:97 offset1:105
	ds_read2_b32 v[76:77], v49 offset0:162 offset1:170
	ds_read2_b32 v[78:79], v49 offset0:227 offset1:235
	ds_read2_b32 v[80:81], v49 offset0:32 offset1:40
	ds_read2_b32 v[82:83], v1 offset0:36 offset1:44
	ds_read2_b32 v[84:85], v1 offset0:101 offset1:109
	ds_read2_b32 v[86:87], v1 offset0:166 offset1:174
	ds_read2_b32 v[88:89], v1 offset0:231 offset1:239
	s_waitcnt lgkmcnt(4)
	v_mul_f32_e32 v75, 0x41800000, v80
	s_waitcnt lgkmcnt(3)
	v_mul_f32_e32 v80, 0x41800000, v82
	s_waitcnt lgkmcnt(2)
	v_mul_f32_e32 v82, 0x41800000, v84
	v_med3_f32 v80, v80, s87, v74
	v_med3_f32 v82, v82, s87, v74
	v_mov_b32_e32 v91, v3
	v_mul_f32_e32 v42, 0x41800000, v42
	v_cvt_pk_fp8_f32 v91, v80, v82
	v_med3_f32 v75, v75, s87, v74
	v_med3_f32 v42, v42, s87, v74
	v_mov_b32_e32 v90, v3
	s_waitcnt lgkmcnt(1)
	v_mul_f32_e32 v84, 0x41800000, v86
	v_cvt_pk_fp8_f32 v90, v75, v42
	s_waitcnt lgkmcnt(0)
	v_mul_f32_e32 v42, 0x41800000, v88
	v_med3_f32 v84, v84, s87, v74
	v_med3_f32 v42, v42, s87, v74
	v_cvt_pk_fp8_f32 v91, v84, v42 op_sel:[0,0,1]
	v_mul_f32_e32 v42, 0x41800000, v81
	v_mul_f32_e32 v76, 0x41800000, v76
	v_mul_f32_e32 v78, 0x41800000, v78
	v_med3_f32 v75, v42, s87, v74
	v_mul_f32_e32 v42, 0x41800000, v43
	v_med3_f32 v76, v76, s87, v74
	v_med3_f32 v78, v78, s87, v74
	v_med3_f32 v43, v42, s87, v74
	v_mul_f32_e32 v42, 0x41800000, v77
	v_cvt_pk_fp8_f32 v90, v76, v78 op_sel:[0,0,1]
	v_med3_f32 v76, v42, s87, v74
	v_mul_f32_e32 v42, 0x41800000, v79
	v_med3_f32 v77, v42, s87, v74
	v_mul_f32_e32 v42, 0x41800000, v83
	v_med3_f32 v78, v42, s87, v74
	v_mul_f32_e32 v42, 0x41800000, v85
	v_med3_f32 v79, v42, s87, v74
	v_mul_f32_e32 v42, 0x41800000, v87
	v_med3_f32 v80, v42, s87, v74
	v_mov_b32_e32 v42, v3
	v_cvt_pk_fp8_f32 v42, v75, v43
	v_mov_b32_e32 v43, v3
	v_cvt_pk_fp8_f32 v43, v78, v79
	v_mul_f32_e32 v75, 0x41800000, v89
	v_med3_f32 v75, v75, s87, v74
	v_add_co_u32_e32 v92, vcc, s89, v40
	v_cvt_pk_fp8_f32 v42, v76, v77 op_sel:[0,0,1]
	v_cvt_pk_fp8_f32 v43, v80, v75 op_sel:[0,0,1]
	v_addc_co_u32_e32 v93, vcc, 0, v41, vcc
	v_add_co_u32_e32 v76, vcc, s93, v40
	global_store_dwordx2 v[92:93], v[90:91], off
	s_nop 0
	v_addc_co_u32_e32 v77, vcc, 0, v41, vcc
	global_store_dwordx2 v[76:77], v[42:43], off
	ds_read2_b32 v[42:43], v49 offset0:113 offset1:121
	ds_read2_b32 v[76:77], v49 offset0:178 offset1:186
	ds_read2_b32 v[78:79], v49 offset0:243 offset1:251
	ds_read2_b32 v[80:81], v49 offset0:48 offset1:56
	ds_read2_b32 v[82:83], v1 offset0:52 offset1:60
	ds_read2_b32 v[84:85], v1 offset0:117 offset1:125
	ds_read2_b32 v[86:87], v1 offset0:182 offset1:190
	ds_read2_b32 v[88:89], v1 offset0:247 offset1:255
	s_waitcnt lgkmcnt(4)
	v_mul_f32_e32 v1, 0x41800000, v80
	v_mul_f32_e32 v42, 0x41800000, v42
	v_med3_f32 v1, v1, s87, v74
	v_med3_f32 v42, v42, s87, v74
	v_mov_b32_e32 v90, v3
	v_cvt_pk_fp8_f32 v90, v1, v42
	v_mul_f32_e32 v75, 0x41800000, v76
	v_mul_f32_e32 v76, 0x41800000, v78
	s_waitcnt lgkmcnt(3)
	v_mul_f32_e32 v78, 0x41800000, v82
	s_waitcnt lgkmcnt(2)
	v_mul_f32_e32 v80, 0x41800000, v84
	v_med3_f32 v78, v78, s87, v74
	v_med3_f32 v80, v80, s87, v74
	v_mov_b32_e32 v91, v3
	v_mul_f32_e32 v42, 0x41800000, v43
	v_med3_f32 v75, v75, s87, v74
	v_med3_f32 v76, v76, s87, v74
	v_cvt_pk_fp8_f32 v91, v78, v80
	v_med3_f32 v43, v42, s87, v74
	v_mul_f32_e32 v42, 0x41800000, v77
	v_cvt_pk_fp8_f32 v90, v75, v76 op_sel:[0,0,1]
	v_med3_f32 v75, v42, s87, v74
	v_mul_f32_e32 v42, 0x41800000, v79
	s_waitcnt lgkmcnt(1)
	v_mul_f32_e32 v82, 0x41800000, v86
	s_waitcnt lgkmcnt(0)
	v_mul_f32_e32 v1, 0x41800000, v88
	v_med3_f32 v76, v42, s87, v74
	v_mul_f32_e32 v42, 0x41800000, v83
	v_med3_f32 v82, v82, s87, v74
	v_med3_f32 v1, v1, s87, v74
	v_med3_f32 v77, v42, s87, v74
	v_mul_f32_e32 v42, 0x41800000, v85
	v_cvt_pk_fp8_f32 v91, v82, v1 op_sel:[0,0,1]
	v_mul_f32_e32 v1, 0x41800000, v81
	v_med3_f32 v78, v42, s87, v74
	v_mul_f32_e32 v42, 0x41800000, v87
	v_med3_f32 v1, v1, s87, v74
	v_med3_f32 v79, v42, s87, v74
	v_mov_b32_e32 v42, v3
	v_cvt_pk_fp8_f32 v42, v1, v43
	v_mov_b32_e32 v43, v3
	v_cvt_pk_fp8_f32 v43, v77, v78
	v_mul_f32_e32 v1, 0x41800000, v89
	v_med3_f32 v1, v1, s87, v74
	v_add_co_u32_e32 v92, vcc, s90, v40
	v_cvt_pk_fp8_f32 v42, v75, v76 op_sel:[0,0,1]
	v_cvt_pk_fp8_f32 v43, v79, v1 op_sel:[0,0,1]
	v_addc_co_u32_e32 v93, vcc, 0, v41, vcc
	v_add_co_u32_e32 v40, vcc, 0x1c000, v40
	global_store_dwordx2 v[92:93], v[90:91], off
	s_nop 0
	v_addc_co_u32_e32 v41, vcc, 0, v41, vcc
	global_store_dwordx2 v[40:41], v[42:43], off
	s_waitcnt lgkmcnt(0)

.LBB0_276:
	s_andn2_b64 vcc, exec, s[2:3]
	s_cbranch_vccnz .LBB0_34
	s_lshl_b32 s2, s8, 6
	s_ashr_i32 s3, s2, 31
	s_sub_i32 s4, 0, s9
	s_lshl_b64 s[8:9], s[2:3], 15
	s_add_u32 s5, s26, s8
	s_addc_u32 s10, s27, s9
	s_lshl_b64 s[8:9], s[34:35], 2
	s_add_u32 s8, s5, s8
	s_addc_u32 s9, s10, s9
	v_lshl_add_u64 v[132:133], s[8:9], 0, v[18:19]
	v_add_co_u32_e32 v76, vcc, s91, v132
	s_mov_b32 s5, 0x80000
	s_nop 0
	v_addc_co_u32_e32 v77, vcc, 0, v133, vcc
	v_add_co_u32_e32 v80, vcc, s1, v132
	global_load_dwordx4 v[40:43], v[132:133], off nt
	s_nop 0
	global_load_dwordx4 v[76:79], v[76:77], off nt
	v_addc_co_u32_e32 v81, vcc, 0, v133, vcc
	v_add_co_u32_e32 v84, vcc, s30, v132
	v_add_u32_e32 v1, 0x410, v48
	s_nop 0
	v_addc_co_u32_e32 v85, vcc, 0, v133, vcc
	global_load_dwordx4 v[80:83], v[80:81], off nt
	s_nop 0
	global_load_dwordx4 v[84:87], v[84:85], off nt
	v_add_co_u32_e32 v88, vcc, s5, v132
	s_mov_b32 s5, 0xa0000
	s_nop 0
	v_addc_co_u32_e32 v89, vcc, 0, v133, vcc
	v_add_co_u32_e32 v92, vcc, s5, v132
	s_mov_b32 s5, 0xc0000
	s_nop 0
	v_addc_co_u32_e32 v93, vcc, 0, v133, vcc
	global_load_dwordx4 v[88:91], v[88:89], off nt
	s_nop 0
	global_load_dwordx4 v[92:95], v[92:93], off nt
	v_add_co_u32_e32 v96, vcc, s5, v132
	s_mov_b32 s5, 0xe0000
	s_nop 0
	v_addc_co_u32_e32 v97, vcc, 0, v133, vcc
	v_add_co_u32_e32 v100, vcc, s5, v132
	s_mov_b32 s5, 0x100000
	s_nop 0
	v_addc_co_u32_e32 v101, vcc, 0, v133, vcc
	global_load_dwordx4 v[96:99], v[96:97], off nt
	s_nop 0
	global_load_dwordx4 v[100:103], v[100:101], off nt
	v_add_co_u32_e32 v104, vcc, s5, v132
	s_mov_b32 s5, 0x120000
	s_nop 0
	v_addc_co_u32_e32 v105, vcc, 0, v133, vcc
	v_add_co_u32_e32 v108, vcc, s5, v132
	s_mov_b32 s5, 0x140000
	s_nop 0
	v_addc_co_u32_e32 v109, vcc, 0, v133, vcc
	global_load_dwordx4 v[104:107], v[104:105], off nt
	s_nop 0
	global_load_dwordx4 v[108:111], v[108:109], off nt
	v_add_co_u32_e32 v112, vcc, s5, v132
	s_mov_b32 s5, 0x160000
	s_nop 0
	v_addc_co_u32_e32 v113, vcc, 0, v133, vcc
	v_add_co_u32_e32 v116, vcc, s5, v132
	s_mov_b32 s5, 0x180000
	s_nop 0
	v_addc_co_u32_e32 v117, vcc, 0, v133, vcc
	global_load_dwordx4 v[112:115], v[112:113], off nt
	s_nop 0
	global_load_dwordx4 v[116:119], v[116:117], off nt
	v_add_co_u32_e32 v120, vcc, s5, v132
	s_mov_b32 s5, 0x1a0000
	s_nop 0
	v_addc_co_u32_e32 v121, vcc, 0, v133, vcc
	v_add_co_u32_e32 v124, vcc, s5, v132
	s_mov_b32 s5, 0x1c0000
	s_nop 0
	v_addc_co_u32_e32 v125, vcc, 0, v133, vcc
	global_load_dwordx4 v[120:123], v[120:121], off nt
	s_nop 0
	global_load_dwordx4 v[124:127], v[124:125], off nt
	v_add_co_u32_e32 v128, vcc, s5, v132
	s_mov_b32 s5, 0x1e0000
	s_nop 0
	v_addc_co_u32_e32 v129, vcc, 0, v133, vcc
	global_load_dwordx4 v[128:131], v[128:129], off nt
	v_add_co_u32_e32 v132, vcc, s5, v132
	s_and_b32 s5, s97, 0x7c0000
	s_nop 0
	v_addc_co_u32_e32 v133, vcc, 0, v133, vcc
	global_load_dwordx4 v[132:135], v[132:133], off nt
	s_waitcnt vmcnt(15)
	ds_write2_b32 v48, v40, v41 offset1:1
	ds_write2_b32 v48, v42, v43 offset0:2 offset1:3
	s_waitcnt vmcnt(14)
	ds_write2_b32 v1, v76, v77 offset1:1
	v_add_u32_e32 v1, 0x418, v48
	ds_write2_b32 v1, v78, v79 offset1:1
	v_add_u32_e32 v1, 0x820, v48
	s_add_u32 s5, s84, s5
	s_addc_u32 s8, s85, 0
	s_add_u32 s2, s5, s2
	s_waitcnt vmcnt(13)
	ds_write2_b32 v1, v80, v81 offset1:1
	v_add_u32_e32 v1, 0x828, v48
	ds_write2_b32 v1, v82, v83 offset1:1
	v_add_u32_e32 v1, 0xc30, v48
	s_waitcnt vmcnt(12)
	ds_write2_b32 v1, v84, v85 offset1:1
	v_add_u32_e32 v1, 0xc38, v48
	ds_write2_b32 v1, v86, v87 offset1:1
	v_add_u32_e32 v1, 0x1040, v48
	v_add_u32_e32 v75, 0x400, v49
	s_addc_u32 s3, s8, s3
	s_add_i32 s4, s4, s95
	s_waitcnt vmcnt(11)
	ds_write2_b32 v1, v88, v89 offset1:1
	v_add_u32_e32 v1, 0x1048, v48
	ds_write2_b32 v1, v90, v91 offset1:1
	v_add_u32_e32 v1, 0x1450, v48
	s_waitcnt vmcnt(10)
	ds_write2_b32 v1, v92, v93 offset1:1
	v_add_u32_e32 v1, 0x1458, v48
	ds_write2_b32 v1, v94, v95 offset1:1
	v_add_u32_e32 v1, 0x1860, v48
	v_mov_b32_e32 v92, v3
	v_mov_b32_e32 v93, v3
	v_lshl_add_u64 v[40:41], s[2:3], 0, v[16:17]
	s_waitcnt vmcnt(9)
	ds_write2_b32 v1, v96, v97 offset1:1
	v_add_u32_e32 v1, 0x1868, v48
	ds_write2_b32 v1, v98, v99 offset1:1
	v_add_u32_e32 v1, 0x1c70, v48
	s_waitcnt vmcnt(8)
	ds_write2_b32 v1, v100, v101 offset1:1
	v_add_u32_e32 v1, 0x1c78, v48
	ds_write2_b32 v1, v102, v103 offset1:1
	v_add_u32_e32 v1, 0x2080, v48
	s_waitcnt vmcnt(7)
	ds_write2_b32 v1, v104, v105 offset1:1
	v_add_u32_e32 v1, 0x2088, v48
	ds_write2_b32 v1, v106, v107 offset1:1
	v_add_u32_e32 v1, 0x2490, v48
	s_waitcnt vmcnt(6)
	ds_write2_b32 v1, v108, v109 offset1:1
	v_add_u32_e32 v1, 0x2498, v48
	ds_write2_b32 v1, v110, v111 offset1:1
	v_add_u32_e32 v1, 0x28a0, v48
	s_waitcnt vmcnt(5)
	ds_write2_b32 v1, v112, v113 offset1:1
	v_add_u32_e32 v1, 0x28a8, v48
	ds_write2_b32 v1, v114, v115 offset1:1
	v_add_u32_e32 v1, 0x2cb0, v48
	s_waitcnt vmcnt(4)
	ds_write2_b32 v1, v116, v117 offset1:1
	v_add_u32_e32 v1, 0x2cb8, v48
	ds_write2_b32 v1, v118, v119 offset1:1
	v_add_u32_e32 v1, 0x30c0, v48
	s_waitcnt vmcnt(3)
	ds_write2_b32 v1, v120, v121 offset1:1
	v_add_u32_e32 v1, 0x30c8, v48
	ds_write2_b32 v1, v122, v123 offset1:1
	v_add_u32_e32 v1, 0x34d0, v48
	s_waitcnt vmcnt(2)
	ds_write2_b32 v1, v124, v125 offset1:1
	v_add_u32_e32 v1, 0x34d8, v48
	ds_write2_b32 v1, v126, v127 offset1:1
	v_add_u32_e32 v1, 0x38e0, v48
	s_waitcnt vmcnt(1)
	ds_write2_b32 v1, v128, v129 offset1:1
	v_add_u32_e32 v1, 0x38e8, v48
	ds_write2_b32 v1, v130, v131 offset1:1
	v_add_u32_e32 v1, 0x3cf0, v48
	s_waitcnt vmcnt(0)
	ds_write2_b32 v1, v132, v133 offset1:1
	v_add_u32_e32 v1, 0x3cf8, v48
	ds_write2_b32 v1, v134, v135 offset1:1
	s_waitcnt lgkmcnt(0)
	ds_read2_b32 v[76:77], v49 offset0:65 offset1:73
	ds_read2_b32 v[78:79], v49 offset0:130 offset1:138
	ds_read2_b32 v[80:81], v49 offset0:195 offset1:203
	ds_read2_b32 v[82:83], v75 offset0:4 offset1:12
	ds_read2_b32 v[84:85], v75 offset0:69 offset1:77
	ds_read2_b32 v[86:87], v49 offset1:8
	ds_read2_b32 v[88:89], v75 offset0:134 offset1:142
	ds_read2_b32 v[90:91], v75 offset0:199 offset1:207
	v_add_u32_e32 v1, s4, v44
	v_and_b32_e32 v1, 0x43, v1
	v_add_u32_e32 v42, v50, v1
	s_waitcnt lgkmcnt(2)
	v_mul_f32_e32 v1, 0x41800000, v86
	v_mul_f32_e32 v43, 0x41800000, v76
	v_med3_f32 v1, v1, s87, v74
	v_med3_f32 v43, v43, s87, v74
	v_cvt_pk_fp8_f32 v92, v1, v43
	v_mul_f32_e32 v76, 0x41800000, v78
	v_mul_f32_e32 v78, 0x41800000, v80
	v_mul_f32_e32 v80, 0x41800000, v82
	v_mul_f32_e32 v82, 0x41800000, v84
	v_med3_f32 v80, v80, s87, v74
	v_med3_f32 v82, v82, s87, v74
	v_med3_f32 v76, v76, s87, v74
	v_med3_f32 v78, v78, s87, v74
	v_cvt_pk_fp8_f32 v93, v80, v82
	v_cvt_pk_fp8_f32 v92, v76, v78 op_sel:[0,0,1]
	v_mul_f32_e32 v78, 0x41800000, v81
	s_waitcnt lgkmcnt(1)
	v_mul_f32_e32 v84, 0x41800000, v88
	s_waitcnt lgkmcnt(0)
	v_mul_f32_e32 v1, 0x41800000, v90
	v_med3_f32 v80, v78, s87, v74
	v_mul_f32_e32 v78, 0x41800000, v83
	v_med3_f32 v84, v84, s87, v74
	v_med3_f32 v1, v1, s87, v74
	v_ashrrev_i32_e32 v43, 31, v42
	v_med3_f32 v81, v78, s87, v74
	v_mul_f32_e32 v78, 0x41800000, v85
	v_cvt_pk_fp8_f32 v93, v84, v1 op_sel:[0,0,1]
	v_lshlrev_b64 v[94:95], 11, v[42:43]
	v_mul_f32_e32 v1, 0x41800000, v87
	v_mul_f32_e32 v43, 0x41800000, v77
	v_med3_f32 v82, v78, s87, v74
	v_mul_f32_e32 v78, 0x41800000, v89
	v_med3_f32 v1, v1, s87, v74
	v_med3_f32 v43, v43, s87, v74
	v_mul_f32_e32 v77, 0x41800000, v79
	v_med3_f32 v83, v78, s87, v74
	v_mov_b32_e32 v78, v3
	v_mov_b32_e32 v79, v3
	v_cvt_pk_fp8_f32 v78, v1, v43
	v_cvt_pk_fp8_f32 v79, v81, v82
	v_mul_f32_e32 v1, 0x41800000, v91
	v_med3_f32 v77, v77, s87, v74
	v_med3_f32 v1, v1, s87, v74
	v_cvt_pk_fp8_f32 v78, v77, v80 op_sel:[0,0,1]
	v_cvt_pk_fp8_f32 v79, v83, v1 op_sel:[0,0,1]
	v_add_u32_e32 v76, 16, v42
	v_mov_b32_e32 v77, v3
	v_lshlrev_b64 v[76:77], 11, v[76:77]
	v_lshl_add_u64 v[94:95], v[40:41], 0, v[94:95]
	v_lshl_add_u64 v[76:77], v[40:41], 0, v[76:77]
	global_store_dwordx2 v[94:95], v[92:93], off
	global_store_dwordx2 v[76:77], v[78:79], off
	ds_read2_b32 v[76:77], v49 offset0:81 offset1:89
	ds_read2_b32 v[78:79], v49 offset0:146 offset1:154
	ds_read2_b32 v[80:81], v49 offset0:211 offset1:219
	ds_read2_b32 v[82:83], v75 offset0:20 offset1:28
	ds_read2_b32 v[84:85], v49 offset0:16 offset1:24
	ds_read2_b32 v[86:87], v75 offset0:85 offset1:93
	ds_read2_b32 v[88:89], v75 offset0:150 offset1:158
	ds_read2_b32 v[90:91], v75 offset0:215 offset1:223
	s_waitcnt lgkmcnt(7)
	v_mul_f32_e32 v43, 0x41800000, v76
	s_waitcnt lgkmcnt(3)
	v_mul_f32_e32 v1, 0x41800000, v84
	v_med3_f32 v1, v1, s87, v74
	v_med3_f32 v43, v43, s87, v74
	v_mov_b32_e32 v94, v3
	v_cvt_pk_fp8_f32 v94, v1, v43
	v_mul_f32_e32 v76, 0x41800000, v78
	v_mul_f32_e32 v78, 0x41800000, v80
	v_mul_f32_e32 v80, 0x41800000, v82
	s_waitcnt lgkmcnt(2)
	v_mul_f32_e32 v82, 0x41800000, v86
	v_med3_f32 v80, v80, s87, v74
	v_med3_f32 v82, v82, s87, v74
	v_mov_b32_e32 v95, v3
	v_med3_f32 v76, v76, s87, v74
	v_med3_f32 v78, v78, s87, v74
	v_cvt_pk_fp8_f32 v95, v80, v82
	v_cvt_pk_fp8_f32 v94, v76, v78 op_sel:[0,0,1]
	v_mul_f32_e32 v78, 0x41800000, v81
	s_waitcnt lgkmcnt(1)
	v_mul_f32_e32 v84, 0x41800000, v88
	s_waitcnt lgkmcnt(0)
	v_mul_f32_e32 v1, 0x41800000, v90
	v_med3_f32 v80, v78, s87, v74
	v_mul_f32_e32 v78, 0x41800000, v83
	v_med3_f32 v84, v84, s87, v74
	v_med3_f32 v1, v1, s87, v74
	v_med3_f32 v81, v78, s87, v74
	v_mul_f32_e32 v78, 0x41800000, v87
	v_cvt_pk_fp8_f32 v95, v84, v1 op_sel:[0,0,1]
	v_mul_f32_e32 v1, 0x41800000, v85
	v_mul_f32_e32 v43, 0x41800000, v77
	v_med3_f32 v82, v78, s87, v74
	v_mul_f32_e32 v78, 0x41800000, v89
	v_med3_f32 v1, v1, s87, v74
	v_med3_f32 v43, v43, s87, v74
	v_mul_f32_e32 v77, 0x41800000, v79
	v_med3_f32 v83, v78, s87, v74
	v_mov_b32_e32 v78, v3
	v_mov_b32_e32 v79, v3
	v_cvt_pk_fp8_f32 v78, v1, v43
	v_cvt_pk_fp8_f32 v79, v81, v82
	v_mul_f32_e32 v1, 0x41800000, v91
	v_med3_f32 v77, v77, s87, v74
	v_med3_f32 v1, v1, s87, v74
	v_cvt_pk_fp8_f32 v78, v77, v80 op_sel:[0,0,1]
	v_cvt_pk_fp8_f32 v79, v83, v1 op_sel:[0,0,1]
	v_add_u32_e32 v92, 32, v42
	v_mov_b32_e32 v93, v3
	v_add_u32_e32 v76, 48, v42
	v_mov_b32_e32 v77, v3
	v_lshlrev_b64 v[92:93], 11, v[92:93]
	v_lshlrev_b64 v[76:77], 11, v[76:77]
	v_lshl_add_u64 v[92:93], v[40:41], 0, v[92:93]
	v_lshl_add_u64 v[76:77], v[40:41], 0, v[76:77]
	global_store_dwordx2 v[92:93], v[94:95], off
	global_store_dwordx2 v[76:77], v[78:79], off
	ds_read2_b32 v[76:77], v49 offset0:97 offset1:105
	ds_read2_b32 v[78:79], v49 offset0:162 offset1:170
	ds_read2_b32 v[80:81], v49 offset0:227 offset1:235
	ds_read2_b32 v[82:83], v75 offset0:36 offset1:44
	ds_read2_b32 v[84:85], v49 offset0:32 offset1:40
	ds_read2_b32 v[86:87], v75 offset0:101 offset1:109
	ds_read2_b32 v[88:89], v75 offset0:166 offset1:174
	ds_read2_b32 v[90:91], v75 offset0:231 offset1:239
	s_waitcnt lgkmcnt(7)
	v_mul_f32_e32 v43, 0x41800000, v76
	s_waitcnt lgkmcnt(3)
	v_mul_f32_e32 v1, 0x41800000, v84
	v_med3_f32 v1, v1, s87, v74
	v_med3_f32 v43, v43, s87, v74
	v_mov_b32_e32 v94, v3
	v_cvt_pk_fp8_f32 v94, v1, v43
	v_mul_f32_e32 v76, 0x41800000, v78
	v_mul_f32_e32 v78, 0x41800000, v80
	v_mul_f32_e32 v80, 0x41800000, v82
	s_waitcnt lgkmcnt(2)
	v_mul_f32_e32 v82, 0x41800000, v86
	v_med3_f32 v80, v80, s87, v74
	v_med3_f32 v82, v82, s87, v74
	v_mov_b32_e32 v95, v3
	v_med3_f32 v76, v76, s87, v74
	v_med3_f32 v78, v78, s87, v74
	v_cvt_pk_fp8_f32 v95, v80, v82
	v_cvt_pk_fp8_f32 v94, v76, v78 op_sel:[0,0,1]
	v_mul_f32_e32 v78, 0x41800000, v81
	s_waitcnt lgkmcnt(1)
	v_mul_f32_e32 v84, 0x41800000, v88
	s_waitcnt lgkmcnt(0)
	v_mul_f32_e32 v1, 0x41800000, v90
	v_med3_f32 v80, v78, s87, v74
	v_mul_f32_e32 v78, 0x41800000, v83
	v_med3_f32 v84, v84, s87, v74
	v_med3_f32 v1, v1, s87, v74
	v_med3_f32 v81, v78, s87, v74
	v_mul_f32_e32 v78, 0x41800000, v87
	v_cvt_pk_fp8_f32 v95, v84, v1 op_sel:[0,0,1]
	v_mul_f32_e32 v1, 0x41800000, v85
	v_mul_f32_e32 v43, 0x41800000, v77
	v_med3_f32 v82, v78, s87, v74
	v_mul_f32_e32 v78, 0x41800000, v89
	v_med3_f32 v1, v1, s87, v74
	v_med3_f32 v43, v43, s87, v74
	v_mul_f32_e32 v77, 0x41800000, v79
	v_med3_f32 v83, v78, s87, v74
	v_mov_b32_e32 v78, v3
	v_mov_b32_e32 v79, v3
	v_cvt_pk_fp8_f32 v78, v1, v43
	v_cvt_pk_fp8_f32 v79, v81, v82
	v_mul_f32_e32 v1, 0x41800000, v91
	v_med3_f32 v77, v77, s87, v74
	v_med3_f32 v1, v1, s87, v74
	v_add_u32_e32 v92, 4, v42
	v_cvt_pk_fp8_f32 v78, v77, v80 op_sel:[0,0,1]
	v_cvt_pk_fp8_f32 v79, v83, v1 op_sel:[0,0,1]
	v_ashrrev_i32_e32 v93, 31, v92
	v_add_u32_e32 v76, 20, v42
	v_mov_b32_e32 v77, v3
	v_lshlrev_b64 v[92:93], 11, v[92:93]
	v_lshlrev_b64 v[76:77], 11, v[76:77]
	v_lshl_add_u64 v[92:93], v[40:41], 0, v[92:93]
	v_lshl_add_u64 v[76:77], v[40:41], 0, v[76:77]
	global_store_dwordx2 v[92:93], v[94:95], off
	global_store_dwordx2 v[76:77], v[78:79], off
	ds_read2_b32 v[76:77], v49 offset0:113 offset1:121
	ds_read2_b32 v[78:79], v49 offset0:178 offset1:186
	ds_read2_b32 v[80:81], v49 offset0:243 offset1:251
	ds_read2_b32 v[82:83], v75 offset0:52 offset1:60
	ds_read2_b32 v[84:85], v49 offset0:48 offset1:56
	ds_read2_b32 v[86:87], v75 offset0:117 offset1:125
	ds_read2_b32 v[88:89], v75 offset0:182 offset1:190
	ds_read2_b32 v[90:91], v75 offset0:247 offset1:255
	s_waitcnt lgkmcnt(7)
	v_mul_f32_e32 v43, 0x41800000, v76
	s_waitcnt lgkmcnt(3)
	v_mul_f32_e32 v1, 0x41800000, v84
	v_med3_f32 v1, v1, s87, v74
	v_med3_f32 v43, v43, s87, v74
	v_mov_b32_e32 v94, v3
	v_cvt_pk_fp8_f32 v94, v1, v43
	v_mul_f32_e32 v75, 0x41800000, v78
	v_mul_f32_e32 v76, 0x41800000, v80
	v_mul_f32_e32 v78, 0x41800000, v82
	s_waitcnt lgkmcnt(2)
	v_mul_f32_e32 v80, 0x41800000, v86
	v_med3_f32 v78, v78, s87, v74
	v_med3_f32 v80, v80, s87, v74
	v_mov_b32_e32 v95, v3
	v_med3_f32 v75, v75, s87, v74
	v_med3_f32 v76, v76, s87, v74
	v_cvt_pk_fp8_f32 v95, v78, v80
	v_cvt_pk_fp8_f32 v94, v75, v76 op_sel:[0,0,1]
	v_mul_f32_e32 v76, 0x41800000, v81
	s_waitcnt lgkmcnt(1)
	v_mul_f32_e32 v82, 0x41800000, v88
	s_waitcnt lgkmcnt(0)
	v_mul_f32_e32 v1, 0x41800000, v90
	v_med3_f32 v78, v76, s87, v74
	v_mul_f32_e32 v76, 0x41800000, v83
	v_med3_f32 v82, v82, s87, v74
	v_med3_f32 v1, v1, s87, v74
	v_mul_f32_e32 v75, 0x41800000, v79
	v_med3_f32 v79, v76, s87, v74
	v_mul_f32_e32 v76, 0x41800000, v87
	v_cvt_pk_fp8_f32 v95, v82, v1 op_sel:[0,0,1]
	v_mul_f32_e32 v1, 0x41800000, v85
	v_mul_f32_e32 v43, 0x41800000, v77
	v_med3_f32 v80, v76, s87, v74
	v_mul_f32_e32 v76, 0x41800000, v89
	v_med3_f32 v1, v1, s87, v74
	v_med3_f32 v43, v43, s87, v74
	v_med3_f32 v81, v76, s87, v74
	v_mov_b32_e32 v76, v3
	v_mov_b32_e32 v77, v3
	v_cvt_pk_fp8_f32 v76, v1, v43
	v_cvt_pk_fp8_f32 v77, v79, v80
	v_mul_f32_e32 v1, 0x41800000, v91
	v_med3_f32 v75, v75, s87, v74
	v_med3_f32 v1, v1, s87, v74
	v_cvt_pk_fp8_f32 v76, v75, v78 op_sel:[0,0,1]
	v_cvt_pk_fp8_f32 v77, v81, v1 op_sel:[0,0,1]
	v_add_u32_e32 v92, 36, v42
	v_mov_b32_e32 v93, v3
	v_add_u32_e32 v42, 52, v42
	v_mov_b32_e32 v43, v3
	v_lshlrev_b64 v[92:93], 11, v[92:93]
	v_lshlrev_b64 v[42:43], 11, v[42:43]
	v_lshl_add_u64 v[92:93], v[40:41], 0, v[92:93]
	v_lshl_add_u64 v[40:41], v[40:41], 0, v[42:43]
	global_store_dwordx2 v[92:93], v[94:95], off
	global_store_dwordx2 v[40:41], v[76:77], off
	s_waitcnt lgkmcnt(0)
	s_branch .LBB0_34
